# attention MFMA segments: one counted lgkmcnt wait now covers up to four hoisted LDS reads (fewer s_waitcnt issue slots between MFMAs); pipeline rebuilt from baseline
# speedup vs baseline: 1.0280x; 1.0032x over previous
.LBB0_528:
	ds_read_b128 v[88:91], v129
	ds_read_b128 v[92:95], v129 offset:1024
	ds_read_b128 v[96:99], v130
	ds_read_b128 v[152:155], v130 offset:1024
	ds_read_b128 v[176:179], v131
	ds_read_b128 v[180:183], v131 offset:1024
	ds_read_b128 v[184:187], v132
	ds_read_b128 v[188:191], v132 offset:1024
	ds_read_b128 v[192:195], v129 offset:8192
	ds_read_b128 v[196:199], v129 offset:9216
	ds_read_b128 v[200:203], v130 offset:8192
	ds_read_b128 v[204:207], v130 offset:9216
	ds_read_b128 v[208:211], v131 offset:8192
	ds_read_b128 v[212:215], v131 offset:9216
	ds_read_b128 v[216:219], v132 offset:8192
	s_and_b64 vcc, exec, s[10:11]
	s_waitcnt lgkmcnt(11)
	v_mfma_f32_16x16x32_bf16 v[72:75], v[88:91], v[0:3], 0
	ds_read_b128 v[220:223], v132 offset:9216
	ds_read_b64_tr_b16 v[224:225], v142 offset:49152
	ds_read_b64_tr_b16 v[226:227], v146 offset:49152
	ds_read_b64_tr_b16 v[230:231], v146 offset:57344
	v_mfma_f32_16x16x32_bf16 v[72:75], v[96:99], v[4:7], v[72:75]
	v_mfma_f32_16x16x32_bf16 v[76:79], v[92:95], v[0:3], 0
	s_waitcnt lgkmcnt(11)
	v_mfma_f32_16x16x32_bf16 v[72:75], v[176:179], v[8:11], v[72:75]
	ds_read_b64_tr_b16 v[228:229], v142 offset:57344
	ds_read_b64_tr_b16 v[88:89], v136 offset:49152
	ds_read_b64_tr_b16 v[90:91], v137 offset:49152
	ds_read_b64_tr_b16 v[98:99], v137 offset:57344
	v_mfma_f32_16x16x32_bf16 v[84:87], v[184:187], v[12:15], v[72:75]
	v_mfma_f32_16x16x32_bf16 v[72:75], v[152:155], v[4:7], v[76:79]
	v_mfma_f32_16x16x32_bf16 v[72:75], v[180:183], v[8:11], v[72:75]
	v_mfma_f32_16x16x32_bf16 v[80:83], v[188:191], v[12:15], v[72:75]
	s_waitcnt lgkmcnt(11)
	s_nop 5
	v_mfma_f32_16x16x32_bf16 v[72:75], v[192:195], v[0:3], 0
	ds_read_b64_tr_b16 v[96:97], v136 offset:57344
	ds_read_b64_tr_b16 v[92:93], v139 offset:49152
	ds_read_b64_tr_b16 v[94:95], v145 offset:49152
	ds_read_b64_tr_b16 v[178:179], v145 offset:57344
	v_mfma_f32_16x16x32_bf16 v[72:75], v[200:203], v[4:7], v[72:75]
	s_waitcnt lgkmcnt(11)
	v_mfma_f32_16x16x32_bf16 v[72:75], v[208:211], v[8:11], v[72:75]
	ds_read_b64_tr_b16 v[176:177], v139 offset:57344
	ds_read_b64_tr_b16 v[184:185], v140 offset:49152
	ds_read_b64_tr_b16 v[186:187], v147 offset:49152
	ds_read_b64_tr_b16 v[154:155], v147 offset:57344
	v_mfma_f32_16x16x32_bf16 v[76:79], v[216:219], v[12:15], v[72:75]
	v_mfma_f32_16x16x32_bf16 v[72:75], v[196:199], v[0:3], 0
	v_mfma_f32_16x16x32_bf16 v[72:75], v[204:207], v[4:7], v[72:75]
	s_waitcnt lgkmcnt(10)
	v_mfma_f32_16x16x32_bf16 v[60:63], v[224:227], v[68:71], v[60:63]
	ds_read_b64_tr_b16 v[152:153], v140 offset:57344
	ds_read_b64_tr_b16 v[180:181], v148 offset:49152
	ds_read_b64_tr_b16 v[182:183], v149 offset:49152
	ds_read_b64_tr_b16 v[190:191], v149 offset:57344
	ds_read_b64_tr_b16 v[188:189], v148 offset:57344
	v_mfma_f32_16x16x32_bf16 v[60:63], v[228:231], v[64:67], v[60:63]
	s_waitcnt lgkmcnt(11)
	v_mfma_f32_16x16x32_bf16 v[52:55], v[88:91], v[68:71], v[52:55]
	ds_read_b64_tr_b16 v[192:193], v133 offset:49152
	ds_read_b64_tr_b16 v[194:195], v134 offset:49152
	ds_read_b64_tr_b16 v[202:203], v134 offset:57344
	ds_read_b64_tr_b16 v[200:201], v133 offset:57344
	v_mfma_f32_16x16x32_bf16 v[52:55], v[96:99], v[64:67], v[52:55]
	s_waitcnt lgkmcnt(11)
	v_mfma_f32_16x16x32_bf16 v[48:51], v[92:95], v[68:71], v[48:51]
	ds_read_b64_tr_b16 v[208:209], v135 offset:49152
	ds_read_b64_tr_b16 v[210:211], v138 offset:49152
	ds_read_b64_tr_b16 v[218:219], v138 offset:57344
	ds_read_b64_tr_b16 v[216:217], v135 offset:57344
	v_mfma_f32_16x16x32_bf16 v[48:51], v[176:179], v[64:67], v[48:51]
	s_waitcnt lgkmcnt(11)
	v_mfma_f32_16x16x32_bf16 v[56:59], v[184:187], v[68:71], v[56:59]
	ds_read_b64_tr_b16 v[196:197], v141 offset:49152
	ds_read_b64_tr_b16 v[198:199], v143 offset:49152
	ds_read_b64_tr_b16 v[206:207], v143 offset:57344
	ds_read_b64_tr_b16 v[204:205], v141 offset:57344
	v_mfma_f32_16x16x32_bf16 v[56:59], v[152:155], v[64:67], v[56:59]
	s_waitcnt lgkmcnt(11)
	v_mfma_f32_16x16x32_bf16 v[32:35], v[180:183], v[68:71], v[32:35]
	v_mfma_f32_16x16x32_bf16 v[32:35], v[188:191], v[64:67], v[32:35]
	s_waitcnt lgkmcnt(7)
	v_mfma_f32_16x16x32_bf16 v[36:39], v[192:195], v[68:71], v[36:39]
	v_mfma_f32_16x16x32_bf16 v[36:39], v[200:203], v[64:67], v[36:39]
	s_waitcnt lgkmcnt(3)
	v_mfma_f32_16x16x32_bf16 v[40:43], v[208:211], v[68:71], v[40:43]
	v_mfma_f32_16x16x32_bf16 v[40:43], v[216:219], v[64:67], v[40:43]
	v_mfma_f32_16x16x32_bf16 v[72:75], v[212:215], v[8:11], v[72:75]
	s_waitcnt lgkmcnt(0)
	v_mfma_f32_16x16x32_bf16 v[44:47], v[196:199], v[68:71], v[44:47]
	v_mfma_f32_16x16x32_bf16 v[72:75], v[220:223], v[12:15], v[72:75]
	v_mfma_f32_16x16x32_bf16 v[44:47], v[204:207], v[64:67], v[44:47]
	s_cbranch_vccnz .LBB0_530
	v_add_u32_e32 v64, 0, v109
	s_waitcnt vmcnt(3)
	ds_write_b128 v100, v[16:19] offset:16384
	s_waitcnt vmcnt(2)
	ds_write_b128 v124, v[20:23] offset:16384
	s_waitcnt vmcnt(1)
	ds_write_b128 v64, v[24:27] offset:32768
	v_add_u32_e32 v64, 0, v112
	s_waitcnt vmcnt(0)
	ds_write_b128 v64, v[28:31] offset:32768

.LBB0_536:
	ds_read_b128 v[168:171], v129 offset:16384
	ds_read_b128 v[172:175], v130 offset:16384
	ds_read_b128 v[176:179], v131 offset:16384
	ds_read_b128 v[180:183], v129 offset:17408
	ds_read_b128 v[184:187], v132 offset:16384
	ds_read_b128 v[188:191], v130 offset:17408
	ds_read_b128 v[192:195], v131 offset:17408
	ds_read_b128 v[196:199], v129 offset:24576
	ds_read_b128 v[200:203], v132 offset:17408
	ds_read_b128 v[204:207], v130 offset:24576
	ds_read_b128 v[208:211], v131 offset:24576
	ds_read_b128 v[212:215], v129 offset:25600
	ds_read_b128 v[216:219], v132 offset:24576
	ds_read_b128 v[220:223], v130 offset:25600
	ds_read_b128 v[224:227], v131 offset:25600
	v_sub_f32_e32 v64, v127, v96
	v_add_f32_e32 v64, v84, v64
	v_exp_f32_e32 v96, v64
	v_sub_f32_e32 v64, v127, v97
	v_add_f32_e32 v64, v85, v64
	v_exp_f32_e32 v97, v64
	v_sub_f32_e32 v64, v127, v98
	v_add_f32_e32 v64, v86, v64
	v_exp_f32_e32 v98, v64
	v_sub_f32_e32 v64, v127, v99
	v_add_f32_e32 v64, v87, v64
	v_exp_f32_e32 v99, v64
	v_sub_f32_e32 v64, v127, v92
	v_add_f32_e32 v64, v80, v64
	v_exp_f32_e32 v153, v64
	v_sub_f32_e32 v64, v127, v93
	v_add_f32_e32 v64, v81, v64
	v_exp_f32_e32 v154, v64
	v_sub_f32_e32 v64, v127, v94
	v_add_f32_e32 v64, v82, v64
	v_exp_f32_e32 v155, v64
	v_sub_f32_e32 v64, v127, v95
	v_add_f32_e32 v64, v83, v64
	s_waitcnt lgkmcnt(11)
	v_mfma_f32_16x16x32_bf16 v[84:87], v[168:171], v[0:3], 0
	ds_read_b128 v[228:231], v132 offset:25600
	ds_read_b64_tr_b16 v[168:169], v142 offset:32768
	ds_read_b64_tr_b16 v[170:171], v146 offset:32768
	v_exp_f32_e32 v156, v64
	v_sub_f32_e32 v64, v127, v88
	v_add_f32_e32 v64, v76, v64
	v_exp_f32_e32 v157, v64
	v_sub_f32_e32 v64, v127, v89
	v_mfma_f32_16x16x32_bf16 v[92:95], v[180:183], v[0:3], 0
	ds_read_b64_tr_b16 v[182:183], v146 offset:40960
	v_add_f32_e32 v64, v77, v64
	v_sub_f32_e32 v70, v127, v67
	v_add_f32_e32 v70, v73, v70
	v_mfma_f32_16x16x32_bf16 v[84:87], v[172:175], v[4:7], v[84:87]
	v_exp_f32_e32 v158, v64
	v_sub_f32_e32 v64, v127, v90
	v_add_f32_e32 v64, v78, v64
	v_exp_f32_e32 v159, v64
	v_sub_f32_e32 v64, v127, v91
	s_waitcnt lgkmcnt(10)
	v_mfma_f32_16x16x32_bf16 v[88:91], v[188:191], v[4:7], v[92:95]
	ds_read_b64_tr_b16 v[180:181], v142 offset:40960
	ds_read_b64_tr_b16 v[172:173], v136 offset:32768
	ds_read_b64_tr_b16 v[174:175], v137 offset:32768
	ds_read_b64_tr_b16 v[190:191], v137 offset:40960
	ds_read_b64_tr_b16 v[188:189], v136 offset:40960
	v_add_f32_e32 v64, v79, v64
	v_exp_f32_e32 v160, v64
	v_sub_f32_e32 v64, v127, v66
	v_mfma_f32_16x16x32_bf16 v[80:83], v[176:179], v[8:11], v[84:87]
	v_add_f32_e32 v64, v72, v64
	v_exp_f32_e32 v161, v64
	v_sub_f32_e32 v68, v127, v68
	v_mfma_f32_16x16x32_bf16 v[76:79], v[192:195], v[8:11], v[88:91]
	v_add_f32_e32 v68, v74, v68
	s_and_b64 vcc, exec, s[10:11]
	v_mfma_f32_16x16x32_bf16 v[92:95], v[196:199], v[0:3], 0
	v_mfma_f32_16x16x32_bf16 v[80:83], v[184:187], v[12:15], v[80:83]
	v_exp_f32_e32 v162, v70
	v_exp_f32_e32 v163, v68
	v_sub_f32_e32 v68, v127, v69
	v_mfma_f32_16x16x32_bf16 v[76:79], v[200:203], v[12:15], v[76:79]
	s_waitcnt lgkmcnt(11)
	v_mfma_f32_16x16x32_bf16 v[88:91], v[204:207], v[4:7], v[92:95]
	ds_read_b64_tr_b16 v[176:177], v139 offset:32768
	ds_read_b64_tr_b16 v[178:179], v145 offset:32768
	ds_read_b64_tr_b16 v[194:195], v145 offset:40960
	ds_read_b64_tr_b16 v[192:193], v139 offset:40960
	v_add_f32_e32 v68, v75, v68
	v_mfma_f32_16x16x32_bf16 v[84:87], v[208:211], v[8:11], v[88:91]
	v_cvt_pk_bf16_f32 v92, v96, v97
	v_cvt_pk_bf16_f32 v93, v98, v99
	v_cvt_pk_bf16_f32 v94, v153, v154
	v_mfma_f32_16x16x32_bf16 v[64:67], v[216:219], v[12:15], v[84:87]
	v_cvt_pk_bf16_f32 v95, v155, v156
	v_mfma_f32_16x16x32_bf16 v[84:87], v[212:215], v[0:3], 0
	v_exp_f32_e32 v164, v68
	s_waitcnt lgkmcnt(11)
	v_mfma_f32_16x16x32_bf16 v[84:87], v[220:223], v[4:7], v[84:87]
	ds_read_b64_tr_b16 v[196:197], v140 offset:32768
	ds_read_b64_tr_b16 v[198:199], v147 offset:32768
	ds_read_b64_tr_b16 v[186:187], v147 offset:40960
	ds_read_b64_tr_b16 v[184:185], v140 offset:40960
	v_mfma_f32_16x16x32_bf16 v[68:71], v[224:227], v[8:11], v[84:87]
	s_nop 2
	v_cvt_pk_bf16_f32 v84, v157, v158
	v_mfma_f32_16x16x32_bf16 v[68:71], v[228:231], v[12:15], v[68:71]
	v_cvt_pk_bf16_f32 v85, v159, v160
	v_cvt_pk_bf16_f32 v86, v161, v162
	s_waitcnt lgkmcnt(11)
	v_mfma_f32_16x16x32_bf16 v[60:63], v[168:171], v[92:95], v[60:63]
	ds_read_b64_tr_b16 v[200:201], v148 offset:32768
	ds_read_b64_tr_b16 v[202:203], v149 offset:32768
	ds_read_b64_tr_b16 v[206:207], v149 offset:40960
	ds_read_b64_tr_b16 v[204:205], v148 offset:40960
	v_cvt_pk_bf16_f32 v87, v163, v164
	s_nop 1
	v_mfma_f32_16x16x32_bf16 v[60:63], v[180:183], v[84:87], v[60:63]
	s_waitcnt lgkmcnt(11)
	v_mfma_f32_16x16x32_bf16 v[52:55], v[172:175], v[92:95], v[52:55]
	ds_read_b64_tr_b16 v[208:209], v133 offset:32768
	ds_read_b64_tr_b16 v[210:211], v134 offset:32768
	ds_read_b64_tr_b16 v[218:219], v134 offset:40960
	ds_read_b64_tr_b16 v[216:217], v133 offset:40960
	v_mfma_f32_16x16x32_bf16 v[52:55], v[188:191], v[84:87], v[52:55]
	s_waitcnt lgkmcnt(11)
	v_mfma_f32_16x16x32_bf16 v[48:51], v[176:179], v[92:95], v[48:51]
	ds_read_b64_tr_b16 v[212:213], v135 offset:32768
	ds_read_b64_tr_b16 v[214:215], v138 offset:32768
	ds_read_b64_tr_b16 v[222:223], v138 offset:40960
	ds_read_b64_tr_b16 v[220:221], v135 offset:40960
	v_mfma_f32_16x16x32_bf16 v[48:51], v[192:195], v[84:87], v[48:51]
	s_waitcnt lgkmcnt(11)
	v_mfma_f32_16x16x32_bf16 v[56:59], v[196:199], v[92:95], v[56:59]
	ds_read_b64_tr_b16 v[224:225], v141 offset:32768
	ds_read_b64_tr_b16 v[226:227], v143 offset:32768
	ds_read_b64_tr_b16 v[230:231], v143 offset:40960
	ds_read_b64_tr_b16 v[228:229], v141 offset:40960
	v_mfma_f32_16x16x32_bf16 v[56:59], v[184:187], v[84:87], v[56:59]
	s_waitcnt lgkmcnt(11)
	v_mfma_f32_16x16x32_bf16 v[32:35], v[200:203], v[92:95], v[32:35]
	v_mfma_f32_16x16x32_bf16 v[32:35], v[204:207], v[84:87], v[32:35]
	s_waitcnt lgkmcnt(7)
	v_mfma_f32_16x16x32_bf16 v[36:39], v[208:211], v[92:95], v[36:39]
	v_mfma_f32_16x16x32_bf16 v[36:39], v[216:219], v[84:87], v[36:39]
	s_waitcnt lgkmcnt(3)
	v_mfma_f32_16x16x32_bf16 v[40:43], v[212:215], v[92:95], v[40:43]
	v_mfma_f32_16x16x32_bf16 v[40:43], v[220:223], v[84:87], v[40:43]
	s_waitcnt lgkmcnt(0)
	v_mfma_f32_16x16x32_bf16 v[44:47], v[224:227], v[92:95], v[44:47]
	v_mfma_f32_16x16x32_bf16 v[44:47], v[228:231], v[84:87], v[44:47]
	s_cbranch_vccnz .LBB0_538
	v_add_u32_e32 v72, 0, v109
	s_waitcnt vmcnt(3)
	ds_write_b128 v100, v[16:19]
	s_waitcnt vmcnt(2)
	ds_write_b128 v124, v[20:23]
	s_waitcnt vmcnt(1)
	ds_write_b128 v72, v[24:27] offset:49152
	v_add_u32_e32 v72, 0, v112
	s_waitcnt vmcnt(0)
	ds_write_b128 v72, v[28:31] offset:49152

.LBB0_567:
	ds_read_b128 v[88:91], v129
	ds_read_b128 v[92:95], v129 offset:1024
	ds_read_b128 v[96:99], v130
	ds_read_b128 v[152:155], v130 offset:1024
	ds_read_b128 v[172:175], v131
	ds_read_b128 v[176:179], v131 offset:1024
	ds_read_b128 v[180:183], v132
	ds_read_b128 v[184:187], v132 offset:1024
	ds_read_b128 v[188:191], v129 offset:8192
	ds_read_b128 v[192:195], v129 offset:9216
	ds_read_b128 v[196:199], v130 offset:8192
	ds_read_b128 v[200:203], v130 offset:9216
	ds_read_b128 v[204:207], v131 offset:8192
	ds_read_b128 v[208:211], v131 offset:9216
	ds_read_b128 v[212:215], v132 offset:8192
	s_and_b64 vcc, exec, s[10:11]
	s_waitcnt lgkmcnt(11)
	v_mfma_f32_16x16x32_bf16 v[72:75], v[88:91], v[0:3], 0
	ds_read_b128 v[216:219], v132 offset:9216
	ds_read_b64_tr_b16 v[220:221], v146 offset:49152
	ds_read_b64_tr_b16 v[222:223], v148 offset:49152
	ds_read_b64_tr_b16 v[226:227], v148 offset:57344
	v_mfma_f32_16x16x32_bf16 v[72:75], v[96:99], v[4:7], v[72:75]
	v_mfma_f32_16x16x32_bf16 v[76:79], v[92:95], v[0:3], 0
	s_waitcnt lgkmcnt(11)
	v_mfma_f32_16x16x32_bf16 v[72:75], v[172:175], v[8:11], v[72:75]
	ds_read_b64_tr_b16 v[224:225], v146 offset:57344
	ds_read_b64_tr_b16 v[228:229], v139 offset:49152
	ds_read_b64_tr_b16 v[230:231], v142 offset:49152
	ds_read_b64_tr_b16 v[90:91], v142 offset:57344
	v_mfma_f32_16x16x32_bf16 v[84:87], v[180:183], v[12:15], v[72:75]
	v_mfma_f32_16x16x32_bf16 v[72:75], v[152:155], v[4:7], v[76:79]
	v_mfma_f32_16x16x32_bf16 v[72:75], v[176:179], v[8:11], v[72:75]
	v_mfma_f32_16x16x32_bf16 v[80:83], v[184:187], v[12:15], v[72:75]
	s_waitcnt lgkmcnt(11)
	s_nop 5
	v_mfma_f32_16x16x32_bf16 v[72:75], v[188:191], v[0:3], 0
	ds_read_b64_tr_b16 v[88:89], v139 offset:57344
	ds_read_b64_tr_b16 v[96:97], v141 offset:49152
	ds_read_b64_tr_b16 v[98:99], v145 offset:49152
	ds_read_b64_tr_b16 v[94:95], v145 offset:57344
	v_mfma_f32_16x16x32_bf16 v[72:75], v[196:199], v[4:7], v[72:75]
	s_waitcnt lgkmcnt(11)
	v_mfma_f32_16x16x32_bf16 v[72:75], v[204:207], v[8:11], v[72:75]
	ds_read_b64_tr_b16 v[92:93], v141 offset:57344
	ds_read_b64_tr_b16 v[172:173], v140 offset:49152
	ds_read_b64_tr_b16 v[174:175], v143 offset:49152
	ds_read_b64_tr_b16 v[182:183], v143 offset:57344
	v_mfma_f32_16x16x32_bf16 v[76:79], v[212:215], v[12:15], v[72:75]
	v_mfma_f32_16x16x32_bf16 v[72:75], v[192:195], v[0:3], 0
	v_mfma_f32_16x16x32_bf16 v[72:75], v[200:203], v[4:7], v[72:75]
	s_waitcnt lgkmcnt(10)
	v_mfma_f32_16x16x32_bf16 v[60:63], v[220:223], v[68:71], v[60:63]
	ds_read_b64_tr_b16 v[180:181], v140 offset:57344
	ds_read_b64_tr_b16 v[152:153], v147 offset:49152
	ds_read_b64_tr_b16 v[154:155], v149 offset:49152
	ds_read_b64_tr_b16 v[178:179], v149 offset:57344
	ds_read_b64_tr_b16 v[176:177], v147 offset:57344
	v_mfma_f32_16x16x32_bf16 v[60:63], v[224:227], v[64:67], v[60:63]
	s_waitcnt lgkmcnt(11)
	v_mfma_f32_16x16x32_bf16 v[56:59], v[228:231], v[68:71], v[56:59]
	ds_read_b64_tr_b16 v[184:185], v133 offset:49152
	ds_read_b64_tr_b16 v[186:187], v134 offset:49152
	ds_read_b64_tr_b16 v[190:191], v134 offset:57344
	ds_read_b64_tr_b16 v[188:189], v133 offset:57344
	v_mfma_f32_16x16x32_bf16 v[56:59], v[88:91], v[64:67], v[56:59]
	s_waitcnt lgkmcnt(11)
	v_mfma_f32_16x16x32_bf16 v[52:55], v[96:99], v[68:71], v[52:55]
	ds_read_b64_tr_b16 v[196:197], v135 offset:49152
	ds_read_b64_tr_b16 v[198:199], v136 offset:49152
	ds_read_b64_tr_b16 v[206:207], v136 offset:57344
	ds_read_b64_tr_b16 v[204:205], v135 offset:57344
	v_mfma_f32_16x16x32_bf16 v[52:55], v[92:95], v[64:67], v[52:55]
	s_waitcnt lgkmcnt(11)
	v_mfma_f32_16x16x32_bf16 v[48:51], v[172:175], v[68:71], v[48:51]
	ds_read_b64_tr_b16 v[212:213], v137 offset:49152
	ds_read_b64_tr_b16 v[214:215], v138 offset:49152
	ds_read_b64_tr_b16 v[194:195], v138 offset:57344
	ds_read_b64_tr_b16 v[192:193], v137 offset:57344
	v_mfma_f32_16x16x32_bf16 v[48:51], v[180:183], v[64:67], v[48:51]
	s_waitcnt lgkmcnt(11)
	v_mfma_f32_16x16x32_bf16 v[32:35], v[152:155], v[68:71], v[32:35]
	v_mfma_f32_16x16x32_bf16 v[32:35], v[176:179], v[64:67], v[32:35]
	s_waitcnt lgkmcnt(7)
	v_mfma_f32_16x16x32_bf16 v[36:39], v[184:187], v[68:71], v[36:39]
	v_mfma_f32_16x16x32_bf16 v[36:39], v[188:191], v[64:67], v[36:39]
	s_waitcnt lgkmcnt(3)
	v_mfma_f32_16x16x32_bf16 v[40:43], v[196:199], v[68:71], v[40:43]
	v_mfma_f32_16x16x32_bf16 v[40:43], v[204:207], v[64:67], v[40:43]
	v_mfma_f32_16x16x32_bf16 v[72:75], v[208:211], v[8:11], v[72:75]
	s_waitcnt lgkmcnt(0)
	v_mfma_f32_16x16x32_bf16 v[44:47], v[212:215], v[68:71], v[44:47]
	v_mfma_f32_16x16x32_bf16 v[72:75], v[216:219], v[12:15], v[72:75]
	v_mfma_f32_16x16x32_bf16 v[44:47], v[192:195], v[64:67], v[44:47]
	s_cbranch_vccnz .LBB0_569
	v_add_u32_e32 v64, 0, v109
	s_waitcnt vmcnt(3)
	ds_write_b128 v100, v[16:19] offset:16384
	s_waitcnt vmcnt(2)
	ds_write_b128 v124, v[20:23] offset:16384
	s_waitcnt vmcnt(1)
	ds_write_b128 v64, v[24:27] offset:32768
	v_add_u32_e32 v64, 0, v112
	s_waitcnt vmcnt(0)
	ds_write_b128 v64, v[28:31] offset:32768

.LBB0_575:
	ds_read_b128 v[164:167], v129 offset:16384
	ds_read_b128 v[168:171], v130 offset:16384
	ds_read_b128 v[172:175], v131 offset:16384
	ds_read_b128 v[176:179], v129 offset:17408
	ds_read_b128 v[180:183], v132 offset:16384
	ds_read_b128 v[184:187], v130 offset:17408
	ds_read_b128 v[188:191], v131 offset:17408
	ds_read_b128 v[192:195], v129 offset:24576
	ds_read_b128 v[196:199], v132 offset:17408
	ds_read_b128 v[200:203], v130 offset:24576
	ds_read_b128 v[204:207], v131 offset:24576
	ds_read_b128 v[208:211], v129 offset:25600
	ds_read_b128 v[212:215], v132 offset:24576
	ds_read_b128 v[216:219], v130 offset:25600
	ds_read_b128 v[220:223], v131 offset:25600
	v_sub_f32_e32 v64, v128, v96
	v_add_f32_e32 v64, v84, v64
	v_exp_f32_e32 v96, v64
	v_sub_f32_e32 v64, v128, v97
	v_add_f32_e32 v64, v85, v64
	v_exp_f32_e32 v97, v64
	v_sub_f32_e32 v64, v128, v98
	v_add_f32_e32 v64, v86, v64
	v_exp_f32_e32 v98, v64
	v_sub_f32_e32 v64, v128, v99
	v_add_f32_e32 v64, v87, v64
	v_exp_f32_e32 v99, v64
	v_sub_f32_e32 v64, v128, v92
	v_add_f32_e32 v64, v80, v64
	v_exp_f32_e32 v152, v64
	v_sub_f32_e32 v64, v128, v93
	v_add_f32_e32 v64, v81, v64
	v_exp_f32_e32 v153, v64
	v_sub_f32_e32 v64, v128, v94
	v_add_f32_e32 v64, v82, v64
	v_exp_f32_e32 v154, v64
	v_sub_f32_e32 v64, v128, v95
	v_add_f32_e32 v64, v83, v64
	s_waitcnt lgkmcnt(11)
	v_mfma_f32_16x16x32_bf16 v[84:87], v[164:167], v[0:3], 0
	ds_read_b128 v[224:227], v132 offset:25600
	ds_read_b64_tr_b16 v[228:229], v146 offset:32768
	ds_read_b64_tr_b16 v[230:231], v148 offset:32768
	ds_read_b64_tr_b16 v[166:167], v148 offset:40960
	v_exp_f32_e32 v155, v64
	v_sub_f32_e32 v64, v128, v88
	v_add_f32_e32 v64, v76, v64
	v_mfma_f32_16x16x32_bf16 v[84:87], v[168:171], v[4:7], v[84:87]
	v_exp_f32_e32 v156, v64
	v_sub_f32_e32 v64, v128, v89
	v_add_f32_e32 v64, v77, v64
	v_mfma_f32_16x16x32_bf16 v[92:95], v[176:179], v[0:3], 0
	v_exp_f32_e32 v157, v64
	v_sub_f32_e32 v64, v128, v90
	v_add_f32_e32 v64, v78, v64
	v_exp_f32_e32 v158, v64
	v_sub_f32_e32 v64, v128, v91
	s_waitcnt lgkmcnt(10)
	v_mfma_f32_16x16x32_bf16 v[88:91], v[184:187], v[4:7], v[92:95]
	ds_read_b64_tr_b16 v[164:165], v146 offset:40960
	ds_read_b64_tr_b16 v[168:169], v139 offset:32768
	ds_read_b64_tr_b16 v[170:171], v142 offset:32768
	ds_read_b64_tr_b16 v[178:179], v142 offset:40960
	ds_read_b64_tr_b16 v[176:177], v139 offset:40960
	v_add_f32_e32 v64, v79, v64
	v_exp_f32_e32 v159, v64
	v_sub_f32_e32 v64, v128, v66
	v_mfma_f32_16x16x32_bf16 v[80:83], v[172:175], v[8:11], v[84:87]
	v_add_f32_e32 v64, v72, v64
	v_sub_f32_e32 v70, v128, v67
	v_add_f32_e32 v70, v73, v70
	v_mfma_f32_16x16x32_bf16 v[76:79], v[188:191], v[8:11], v[88:91]
	v_sub_f32_e32 v68, v128, v68
	v_add_f32_e32 v68, v74, v68
	s_and_b64 vcc, exec, s[10:11]
	v_mfma_f32_16x16x32_bf16 v[92:95], v[192:195], v[0:3], 0
	v_mfma_f32_16x16x32_bf16 v[76:79], v[196:199], v[12:15], v[76:79]
	s_waitcnt lgkmcnt(11)
	v_mfma_f32_16x16x32_bf16 v[88:91], v[200:203], v[4:7], v[92:95]
	ds_read_b64_tr_b16 v[184:185], v141 offset:32768
	ds_read_b64_tr_b16 v[186:187], v145 offset:32768
	ds_read_b64_tr_b16 v[174:175], v145 offset:40960
	ds_read_b64_tr_b16 v[172:173], v141 offset:40960
	v_mfma_f32_16x16x32_bf16 v[80:83], v[180:183], v[12:15], v[80:83]
	v_exp_f32_e32 v160, v64
	v_exp_f32_e32 v161, v70
	v_mfma_f32_16x16x32_bf16 v[84:87], v[204:207], v[8:11], v[88:91]
	v_exp_f32_e32 v162, v68
	v_sub_f32_e32 v68, v128, v69
	v_mfma_f32_16x16x32_bf16 v[64:67], v[212:215], v[12:15], v[84:87]
	v_add_f32_e32 v68, v75, v68
	v_exp_f32_e32 v163, v68
	v_mfma_f32_16x16x32_bf16 v[84:87], v[208:211], v[0:3], 0
	v_cvt_pk_bf16_f32 v92, v96, v97
	v_cvt_pk_bf16_f32 v93, v98, v99
	s_waitcnt lgkmcnt(11)
	v_mfma_f32_16x16x32_bf16 v[84:87], v[216:219], v[4:7], v[84:87]
	ds_read_b64_tr_b16 v[188:189], v140 offset:32768
	ds_read_b64_tr_b16 v[190:191], v143 offset:32768
	ds_read_b64_tr_b16 v[194:195], v143 offset:40960
	ds_read_b64_tr_b16 v[192:193], v140 offset:40960
	v_cvt_pk_bf16_f32 v94, v152, v153
	v_cvt_pk_bf16_f32 v95, v154, v155
	v_mfma_f32_16x16x32_bf16 v[68:71], v[220:223], v[8:11], v[84:87]
	s_nop 2
	v_cvt_pk_bf16_f32 v84, v156, v157
	v_mfma_f32_16x16x32_bf16 v[68:71], v[224:227], v[12:15], v[68:71]
	v_cvt_pk_bf16_f32 v85, v158, v159
	v_cvt_pk_bf16_f32 v86, v160, v161
	s_waitcnt lgkmcnt(11)
	v_mfma_f32_16x16x32_bf16 v[60:63], v[228:231], v[92:95], v[60:63]
	ds_read_b64_tr_b16 v[196:197], v147 offset:32768
	ds_read_b64_tr_b16 v[198:199], v149 offset:32768
	ds_read_b64_tr_b16 v[202:203], v149 offset:40960
	ds_read_b64_tr_b16 v[200:201], v147 offset:40960
	v_cvt_pk_bf16_f32 v87, v162, v163
	s_nop 1
	v_mfma_f32_16x16x32_bf16 v[60:63], v[164:167], v[84:87], v[60:63]
	s_waitcnt lgkmcnt(11)
	v_mfma_f32_16x16x32_bf16 v[56:59], v[168:171], v[92:95], v[56:59]
	ds_read_b64_tr_b16 v[180:181], v133 offset:32768
	ds_read_b64_tr_b16 v[182:183], v134 offset:32768
	ds_read_b64_tr_b16 v[206:207], v134 offset:40960
	ds_read_b64_tr_b16 v[204:205], v133 offset:40960
	v_mfma_f32_16x16x32_bf16 v[56:59], v[176:179], v[84:87], v[56:59]
	s_waitcnt lgkmcnt(11)
	v_mfma_f32_16x16x32_bf16 v[52:55], v[184:187], v[92:95], v[52:55]
	ds_read_b64_tr_b16 v[212:213], v135 offset:32768
	ds_read_b64_tr_b16 v[214:215], v136 offset:32768
	ds_read_b64_tr_b16 v[210:211], v136 offset:40960
	ds_read_b64_tr_b16 v[208:209], v135 offset:40960
	v_mfma_f32_16x16x32_bf16 v[52:55], v[172:175], v[84:87], v[52:55]
	s_waitcnt lgkmcnt(11)
	v_mfma_f32_16x16x32_bf16 v[48:51], v[188:191], v[92:95], v[48:51]
	ds_read_b64_tr_b16 v[216:217], v137 offset:32768
	ds_read_b64_tr_b16 v[218:219], v138 offset:32768
	ds_read_b64_tr_b16 v[222:223], v138 offset:40960
	ds_read_b64_tr_b16 v[220:221], v137 offset:40960
	v_mfma_f32_16x16x32_bf16 v[48:51], v[192:195], v[84:87], v[48:51]
	s_waitcnt lgkmcnt(11)
	v_mfma_f32_16x16x32_bf16 v[32:35], v[196:199], v[92:95], v[32:35]
	v_mfma_f32_16x16x32_bf16 v[32:35], v[200:203], v[84:87], v[32:35]
	s_waitcnt lgkmcnt(7)
	v_mfma_f32_16x16x32_bf16 v[36:39], v[180:183], v[92:95], v[36:39]
	v_mfma_f32_16x16x32_bf16 v[36:39], v[204:207], v[84:87], v[36:39]
	s_waitcnt lgkmcnt(3)
	v_mfma_f32_16x16x32_bf16 v[40:43], v[212:215], v[92:95], v[40:43]
	v_mfma_f32_16x16x32_bf16 v[40:43], v[208:211], v[84:87], v[40:43]
	s_waitcnt lgkmcnt(0)
	v_mfma_f32_16x16x32_bf16 v[44:47], v[216:219], v[92:95], v[44:47]
	v_mfma_f32_16x16x32_bf16 v[44:47], v[220:223], v[84:87], v[44:47]
	s_cbranch_vccnz .LBB0_577
	v_add_u32_e32 v72, 0, v109
	s_waitcnt vmcnt(3)
	ds_write_b128 v100, v[16:19]
	s_waitcnt vmcnt(2)
	ds_write_b128 v124, v[20:23]
	s_waitcnt vmcnt(1)
	ds_write_b128 v72, v[24:27] offset:49152
	v_add_u32_e32 v72, 0, v112
	s_waitcnt vmcnt(0)
	ds_write_b128 v72, v[28:31] offset:49152

.LBB0_639:
	ds_read_b128 v[88:91], v128
	ds_read_b128 v[92:95], v128 offset:1024
	ds_read_b128 v[156:159], v129
	ds_read_b128 v[188:191], v129 offset:1024
	ds_read_b128 v[192:195], v130
	ds_read_b128 v[196:199], v130 offset:1024
	ds_read_b128 v[200:203], v131
	ds_read_b128 v[204:207], v131 offset:1024
	ds_read_b128 v[208:211], v128 offset:8192
	ds_read_b128 v[212:215], v128 offset:9216
	ds_read_b128 v[216:219], v129 offset:8192
	ds_read_b128 v[220:223], v129 offset:9216
	ds_read_b128 v[224:227], v130 offset:8192
	ds_read_b128 v[228:231], v130 offset:9216
	s_and_b64 vcc, exec, s[10:11]
	s_waitcnt lgkmcnt(10)
	v_mfma_f32_16x16x32_bf16 v[72:75], v[88:91], v[0:3], 0
	ds_read_b128 v[88:91], v131 offset:8192
	v_mfma_f32_16x16x32_bf16 v[80:83], v[92:95], v[0:3], 0
	ds_read_b128 v[92:95], v131 offset:9216
	v_mfma_f32_16x16x32_bf16 v[72:75], v[156:159], v[4:7], v[72:75]
	ds_read_b64_tr_b16 v[156:157], v140 offset:49152
	ds_read_b64_tr_b16 v[158:159], v141 offset:49152
	s_waitcnt lgkmcnt(10)
	v_mfma_f32_16x16x32_bf16 v[72:75], v[192:195], v[8:11], v[72:75]
	ds_read_b64_tr_b16 v[194:195], v141 offset:57344
	ds_read_b64_tr_b16 v[192:193], v140 offset:57344
	v_mfma_f32_16x16x32_bf16 v[76:79], v[200:203], v[12:15], v[72:75]
	ds_read_b64_tr_b16 v[200:201], v136 offset:49152
	ds_read_b64_tr_b16 v[202:203], v137 offset:49152
	v_mfma_f32_16x16x32_bf16 v[72:75], v[188:191], v[4:7], v[80:83]
	ds_read_b64_tr_b16 v[190:191], v137 offset:57344
	v_mfma_f32_16x16x32_bf16 v[72:75], v[196:199], v[8:11], v[72:75]
	v_mfma_f32_16x16x32_bf16 v[72:75], v[204:207], v[12:15], v[72:75]
	s_waitcnt lgkmcnt(11)
	v_mfma_f32_16x16x32_bf16 v[80:83], v[208:211], v[0:3], 0
	ds_read_b64_tr_b16 v[188:189], v136 offset:57344
	ds_read_b64_tr_b16 v[196:197], v138 offset:49152
	ds_read_b64_tr_b16 v[198:199], v142 offset:49152
	ds_read_b64_tr_b16 v[206:207], v142 offset:57344
	v_mfma_f32_16x16x32_bf16 v[80:83], v[216:219], v[4:7], v[80:83]
	s_waitcnt lgkmcnt(11)
	v_mfma_f32_16x16x32_bf16 v[80:83], v[224:227], v[8:11], v[80:83]
	ds_read_b64_tr_b16 v[204:205], v138 offset:57344
	ds_read_b64_tr_b16 v[208:209], v139 offset:49152
	ds_read_b64_tr_b16 v[210:211], v143 offset:49152
	ds_read_b64_tr_b16 v[218:219], v143 offset:57344
	v_mfma_f32_16x16x32_bf16 v[84:87], v[88:91], v[12:15], v[80:83]
	v_mfma_f32_16x16x32_bf16 v[80:83], v[212:215], v[0:3], 0
	v_mfma_f32_16x16x32_bf16 v[80:83], v[220:223], v[4:7], v[80:83]
	s_waitcnt lgkmcnt(10)
	v_mfma_f32_16x16x32_bf16 v[48:51], v[156:159], v[68:71], v[48:51]
	ds_read_b64_tr_b16 v[216:217], v139 offset:57344
	ds_read_b64_tr_b16 v[224:225], v145 offset:49152
	ds_read_b64_tr_b16 v[226:227], v146 offset:49152
	ds_read_b64_tr_b16 v[90:91], v146 offset:57344
	ds_read_b64_tr_b16 v[88:89], v145 offset:57344
	v_mfma_f32_16x16x32_bf16 v[48:51], v[192:195], v[64:67], v[48:51]
	s_waitcnt lgkmcnt(11)
	v_mfma_f32_16x16x32_bf16 v[40:43], v[200:203], v[68:71], v[40:43]
	ds_read_b64_tr_b16 v[212:213], v147 offset:49152
	ds_read_b64_tr_b16 v[214:215], v148 offset:49152
	ds_read_b64_tr_b16 v[222:223], v148 offset:57344
	ds_read_b64_tr_b16 v[220:221], v147 offset:57344
	v_mfma_f32_16x16x32_bf16 v[40:43], v[188:191], v[64:67], v[40:43]
	s_waitcnt lgkmcnt(11)
	v_mfma_f32_16x16x32_bf16 v[44:47], v[196:199], v[68:71], v[44:47]
	ds_read_b64_tr_b16 v[156:157], v149 offset:49152
	ds_read_b64_tr_b16 v[158:159], v150 offset:49152
	ds_read_b64_tr_b16 v[194:195], v150 offset:57344
	ds_read_b64_tr_b16 v[192:193], v149 offset:57344
	v_mfma_f32_16x16x32_bf16 v[44:47], v[204:207], v[64:67], v[44:47]
	s_waitcnt lgkmcnt(11)
	v_mfma_f32_16x16x32_bf16 v[56:59], v[208:211], v[68:71], v[56:59]
	ds_read_b64_tr_b16 v[200:201], v151 offset:49152
	ds_read_b64_tr_b16 v[202:203], v152 offset:49152
	ds_read_b64_tr_b16 v[190:191], v152 offset:57344
	ds_read_b64_tr_b16 v[188:189], v151 offset:57344
	v_mfma_f32_16x16x32_bf16 v[56:59], v[216:219], v[64:67], v[56:59]
	s_waitcnt lgkmcnt(11)
	v_mfma_f32_16x16x32_bf16 v[60:63], v[224:227], v[68:71], v[60:63]
	v_mfma_f32_16x16x32_bf16 v[60:63], v[88:91], v[64:67], v[60:63]
	s_waitcnt lgkmcnt(7)
	v_mfma_f32_16x16x32_bf16 v[52:55], v[212:215], v[68:71], v[52:55]
	v_mfma_f32_16x16x32_bf16 v[52:55], v[220:223], v[64:67], v[52:55]
	s_waitcnt lgkmcnt(3)
	v_mfma_f32_16x16x32_bf16 v[32:35], v[156:159], v[68:71], v[32:35]
	v_mfma_f32_16x16x32_bf16 v[32:35], v[192:195], v[64:67], v[32:35]
	v_mfma_f32_16x16x32_bf16 v[80:83], v[228:231], v[8:11], v[80:83]
	s_waitcnt lgkmcnt(0)
	v_mfma_f32_16x16x32_bf16 v[36:39], v[200:203], v[68:71], v[36:39]
	v_mfma_f32_16x16x32_bf16 v[80:83], v[92:95], v[12:15], v[80:83]
	v_mfma_f32_16x16x32_bf16 v[36:39], v[188:191], v[64:67], v[36:39]
	s_cbranch_vccnz .LBB0_641
	s_waitcnt vmcnt(3)
	ds_write_b128 v98, v[16:19] offset:16384
	s_waitcnt vmcnt(2)
	ds_write_b128 v99, v[20:23] offset:16384
	s_waitcnt vmcnt(1)
	ds_write_b128 v100, v[24:27] offset:32768
	s_waitcnt vmcnt(0)
	ds_write_b128 v124, v[28:31] offset:32768

.LBB0_663:
	ds_read_b128 v[176:179], v128 offset:16384
	ds_read_b128 v[180:183], v128 offset:17408
	ds_read_b128 v[188:191], v129 offset:16384
	ds_read_b128 v[192:195], v130 offset:16384
	ds_read_b128 v[196:199], v131 offset:16384
	ds_read_b128 v[200:203], v129 offset:17408
	ds_read_b128 v[204:207], v130 offset:17408
	ds_read_b128 v[208:211], v129 offset:24576
	ds_read_b128 v[212:215], v131 offset:17408
	ds_read_b128 v[216:219], v128 offset:24576
	ds_read_b128 v[220:223], v130 offset:24576
	ds_read_b128 v[224:227], v128 offset:25600
	ds_read_b128 v[228:231], v131 offset:24576
	v_pk_mul_f32 v[184:185], v[66:67], v[68:69]
	s_waitcnt lgkmcnt(9)
	v_mfma_f32_16x16x32_bf16 v[160:163], v[176:179], v[0:3], 0
	ds_read_b128 v[176:179], v129 offset:25600
	v_mul_f32_e32 v70, v70, v71
	v_mul_f32_e32 v157, v70, v157
	v_mul_f32_e32 v159, v157, v159
	v_mfma_f32_16x16x32_bf16 v[164:167], v[180:183], v[0:3], 0
	ds_read_b128 v[180:183], v130 offset:25600
	v_mul_f32_e32 v186, v153, v159
	v_pk_mul_f32 v[64:65], v[64:65], v[96:97]
	v_pk_mul_f32 v[72:73], v[72:73], v[74:75]
	v_mfma_f32_16x16x32_bf16 v[160:163], v[188:191], v[4:7], v[160:163]
	ds_read_b128 v[188:191], v131 offset:25600
	v_pk_mul_f32 v[96:97], v[64:65], v[186:187] op_sel_hi:[1,0]
	v_pk_mul_f32 v[84:85], v[84:85], v[94:95]
	v_mfma_f32_16x16x32_bf16 v[66:69], v[192:195], v[8:11], v[160:163]
	ds_read_b64_tr_b16 v[192:193], v140 offset:32768
	ds_read_b64_tr_b16 v[194:195], v141 offset:32768
	v_cvt_pk_bf16_f32 v173, v96, v97
	v_pk_mul_f32 v[96:97], v[76:77], v[78:79]
	s_waitcnt lgkmcnt(10)
	v_mfma_f32_16x16x32_bf16 v[68:71], v[196:199], v[12:15], v[66:69]
	ds_read_b64_tr_b16 v[198:199], v141 offset:40960
	ds_read_b64_tr_b16 v[196:197], v140 offset:40960
	v_pk_mul_f32 v[96:97], v[96:97], v[186:187] op_sel_hi:[1,0]
	v_pk_mul_f32 v[86:87], v[86:87], v[92:93]
	v_mfma_f32_16x16x32_bf16 v[164:167], v[200:203], v[4:7], v[164:167]
	ds_read_b64_tr_b16 v[200:201], v136 offset:32768
	ds_read_b64_tr_b16 v[202:203], v137 offset:32768
	v_mul_f32_e64 v66, v184, v186
	v_mul_f32_e64 v67, v185, v186
	v_pk_mul_f32 v[80:81], v[80:81], v[82:83]
	v_cvt_pk_bf16_f32 v172, v66, v67
	v_mfma_f32_16x16x32_bf16 v[64:67], v[204:207], v[8:11], v[164:167]
	ds_read_b64_tr_b16 v[206:207], v137 offset:40960
	s_and_b64 vcc, exec, s[10:11]
	s_waitcnt lgkmcnt(11)
	v_mfma_f32_16x16x32_bf16 v[64:67], v[212:215], v[12:15], v[64:67]
	ds_read_b64_tr_b16 v[204:205], v136 offset:40960
	ds_read_b64_tr_b16 v[212:213], v138 offset:32768
	ds_read_b64_tr_b16 v[214:215], v142 offset:32768
	v_mfma_f32_16x16x32_bf16 v[168:171], v[216:219], v[0:3], 0
	ds_read_b64_tr_b16 v[218:219], v142 offset:40960
	v_cvt_pk_bf16_f32 v174, v96, v97
	v_pk_mul_f32 v[96:97], v[72:73], v[186:187] op_sel_hi:[1,0]
	v_mfma_f32_16x16x32_bf16 v[76:79], v[208:211], v[4:7], v[168:171]
	v_cvt_pk_bf16_f32 v175, v96, v97
	v_mfma_f32_16x16x32_bf16 v[94:97], v[224:227], v[0:3], 0
	v_mfma_f32_16x16x32_bf16 v[72:75], v[220:223], v[8:11], v[76:79]
	v_mul_f32_e32 v162, v153, v158
	v_pk_mul_f32 v[84:85], v[84:85], v[162:163] op_sel_hi:[1,0]
	v_pk_mul_f32 v[86:87], v[86:87], v[162:163] op_sel_hi:[1,0]
	s_waitcnt lgkmcnt(10)
	v_mfma_f32_16x16x32_bf16 v[92:95], v[176:179], v[4:7], v[94:97]
	ds_read_b64_tr_b16 v[216:217], v138 offset:40960
	ds_read_b64_tr_b16 v[208:209], v139 offset:32768
	ds_read_b64_tr_b16 v[210:211], v143 offset:32768
	ds_read_b64_tr_b16 v[226:227], v143 offset:40960
	ds_read_b64_tr_b16 v[224:225], v139 offset:40960
	v_cvt_pk_bf16_f32 v84, v84, v85
	v_cvt_pk_bf16_f32 v85, v86, v87
	v_pk_mul_f32 v[86:87], v[88:89], v[90:91]
	v_mfma_f32_16x16x32_bf16 v[92:95], v[180:183], v[8:11], v[92:95]
	v_pk_mul_f32 v[86:87], v[86:87], v[162:163] op_sel_hi:[1,0]
	v_mfma_f32_16x16x32_bf16 v[76:79], v[188:191], v[12:15], v[92:95]
	v_cvt_pk_bf16_f32 v86, v86, v87
	s_nop 4
	v_pk_mul_f32 v[92:93], v[80:81], v[162:163] op_sel_hi:[1,0]
	s_waitcnt lgkmcnt(11)
	v_mfma_f32_16x16x32_bf16 v[48:51], v[192:195], v[172:175], v[48:51]
	ds_read_b64_tr_b16 v[220:221], v145 offset:32768
	ds_read_b64_tr_b16 v[222:223], v146 offset:32768
	ds_read_b64_tr_b16 v[178:179], v146 offset:40960
	ds_read_b64_tr_b16 v[176:177], v145 offset:40960
	v_cvt_pk_bf16_f32 v87, v92, v93
	s_waitcnt lgkmcnt(11)
	v_mfma_f32_16x16x32_bf16 v[40:43], v[200:203], v[172:175], v[40:43]
	ds_read_b64_tr_b16 v[180:181], v147 offset:32768
	ds_read_b64_tr_b16 v[182:183], v148 offset:32768
	ds_read_b64_tr_b16 v[190:191], v148 offset:40960
	ds_read_b64_tr_b16 v[188:189], v147 offset:40960
	v_mfma_f32_16x16x32_bf16 v[40:43], v[204:207], v[84:87], v[40:43]
	s_waitcnt lgkmcnt(11)
	v_mfma_f32_16x16x32_bf16 v[44:47], v[212:215], v[172:175], v[44:47]
	ds_read_b64_tr_b16 v[192:193], v149 offset:32768
	ds_read_b64_tr_b16 v[194:195], v150 offset:32768
	ds_read_b64_tr_b16 v[202:203], v150 offset:40960
	ds_read_b64_tr_b16 v[200:201], v149 offset:40960
	v_mfma_f32_16x16x32_bf16 v[44:47], v[216:219], v[84:87], v[44:47]
	s_waitcnt lgkmcnt(11)
	v_mfma_f32_16x16x32_bf16 v[56:59], v[208:211], v[172:175], v[56:59]
	ds_read_b64_tr_b16 v[204:205], v151 offset:32768
	ds_read_b64_tr_b16 v[206:207], v152 offset:32768
	ds_read_b64_tr_b16 v[214:215], v152 offset:40960
	ds_read_b64_tr_b16 v[212:213], v151 offset:40960
	v_mfma_f32_16x16x32_bf16 v[56:59], v[224:227], v[84:87], v[56:59]
	s_waitcnt lgkmcnt(11)
	v_mfma_f32_16x16x32_bf16 v[60:63], v[220:223], v[172:175], v[60:63]
	v_mfma_f32_16x16x32_bf16 v[60:63], v[176:179], v[84:87], v[60:63]
	s_waitcnt lgkmcnt(7)
	v_mfma_f32_16x16x32_bf16 v[52:55], v[180:183], v[172:175], v[52:55]
	v_mfma_f32_16x16x32_bf16 v[52:55], v[188:191], v[84:87], v[52:55]
	s_waitcnt lgkmcnt(3)
	v_mfma_f32_16x16x32_bf16 v[32:35], v[192:195], v[172:175], v[32:35]
	v_mfma_f32_16x16x32_bf16 v[32:35], v[200:203], v[84:87], v[32:35]
	s_waitcnt lgkmcnt(0)
	v_mfma_f32_16x16x32_bf16 v[36:39], v[204:207], v[172:175], v[36:39]
	v_mfma_f32_16x16x32_bf16 v[72:75], v[228:231], v[12:15], v[72:75]
	v_mfma_f32_16x16x32_bf16 v[48:51], v[196:199], v[84:87], v[48:51]
	v_mfma_f32_16x16x32_bf16 v[36:39], v[212:215], v[84:87], v[36:39]
	s_cbranch_vccnz .LBB0_665
	s_waitcnt vmcnt(3)
	ds_write_b128 v98, v[16:19]
	s_waitcnt vmcnt(2)
	ds_write_b128 v99, v[20:23]
	s_waitcnt vmcnt(1)
	ds_write_b128 v100, v[24:27] offset:49152
	s_waitcnt vmcnt(0)
	ds_write_b128 v124, v[28:31] offset:49152

.LBB0_742:
	ds_read_b128 v[88:91], v128
	ds_read_b128 v[92:95], v128 offset:1024
	ds_read_b128 v[156:159], v129
	ds_read_b128 v[188:191], v129 offset:1024
	ds_read_b128 v[192:195], v130
	ds_read_b128 v[196:199], v130 offset:1024
	ds_read_b128 v[200:203], v131
	ds_read_b128 v[204:207], v131 offset:1024
	ds_read_b128 v[208:211], v128 offset:8192
	ds_read_b128 v[212:215], v128 offset:9216
	ds_read_b128 v[216:219], v129 offset:8192
	ds_read_b128 v[220:223], v129 offset:9216
	ds_read_b128 v[224:227], v130 offset:8192
	ds_read_b128 v[228:231], v130 offset:9216
	s_and_b64 vcc, exec, s[10:11]
	s_waitcnt lgkmcnt(10)
	v_mfma_f32_16x16x32_bf16 v[72:75], v[88:91], v[0:3], 0
	ds_read_b128 v[88:91], v131 offset:8192
	v_mfma_f32_16x16x32_bf16 v[80:83], v[92:95], v[0:3], 0
	ds_read_b128 v[92:95], v131 offset:9216
	v_mfma_f32_16x16x32_bf16 v[72:75], v[156:159], v[4:7], v[72:75]
	ds_read_b64_tr_b16 v[156:157], v142 offset:49152
	ds_read_b64_tr_b16 v[158:159], v143 offset:49152
	s_waitcnt lgkmcnt(10)
	v_mfma_f32_16x16x32_bf16 v[72:75], v[192:195], v[8:11], v[72:75]
	ds_read_b64_tr_b16 v[194:195], v143 offset:57344
	ds_read_b64_tr_b16 v[192:193], v142 offset:57344
	v_mfma_f32_16x16x32_bf16 v[76:79], v[200:203], v[12:15], v[72:75]
	ds_read_b64_tr_b16 v[200:201], v136 offset:49152
	ds_read_b64_tr_b16 v[202:203], v139 offset:49152
	v_mfma_f32_16x16x32_bf16 v[72:75], v[188:191], v[4:7], v[80:83]
	ds_read_b64_tr_b16 v[190:191], v139 offset:57344
	v_mfma_f32_16x16x32_bf16 v[72:75], v[196:199], v[8:11], v[72:75]
	v_mfma_f32_16x16x32_bf16 v[72:75], v[204:207], v[12:15], v[72:75]
	s_waitcnt lgkmcnt(11)
	v_mfma_f32_16x16x32_bf16 v[80:83], v[208:211], v[0:3], 0
	ds_read_b64_tr_b16 v[188:189], v136 offset:57344
	ds_read_b64_tr_b16 v[196:197], v138 offset:49152
	ds_read_b64_tr_b16 v[198:199], v141 offset:49152
	ds_read_b64_tr_b16 v[206:207], v141 offset:57344
	v_mfma_f32_16x16x32_bf16 v[80:83], v[216:219], v[4:7], v[80:83]
	s_waitcnt lgkmcnt(11)
	v_mfma_f32_16x16x32_bf16 v[80:83], v[224:227], v[8:11], v[80:83]
	ds_read_b64_tr_b16 v[204:205], v138 offset:57344
	ds_read_b64_tr_b16 v[208:209], v137 offset:49152
	ds_read_b64_tr_b16 v[210:211], v140 offset:49152
	ds_read_b64_tr_b16 v[218:219], v140 offset:57344
	v_mfma_f32_16x16x32_bf16 v[84:87], v[88:91], v[12:15], v[80:83]
	v_mfma_f32_16x16x32_bf16 v[80:83], v[212:215], v[0:3], 0
	v_mfma_f32_16x16x32_bf16 v[80:83], v[220:223], v[4:7], v[80:83]
	s_waitcnt lgkmcnt(10)
	v_mfma_f32_16x16x32_bf16 v[60:63], v[156:159], v[64:67], v[60:63]
	ds_read_b64_tr_b16 v[216:217], v137 offset:57344
	ds_read_b64_tr_b16 v[224:225], v145 offset:49152
	ds_read_b64_tr_b16 v[226:227], v146 offset:49152
	ds_read_b64_tr_b16 v[90:91], v146 offset:57344
	ds_read_b64_tr_b16 v[88:89], v145 offset:57344
	v_mfma_f32_16x16x32_bf16 v[60:63], v[192:195], v[68:71], v[60:63]
	s_waitcnt lgkmcnt(11)
	v_mfma_f32_16x16x32_bf16 v[52:55], v[200:203], v[64:67], v[52:55]
	ds_read_b64_tr_b16 v[212:213], v147 offset:49152
	ds_read_b64_tr_b16 v[214:215], v148 offset:49152
	ds_read_b64_tr_b16 v[222:223], v148 offset:57344
	ds_read_b64_tr_b16 v[220:221], v147 offset:57344
	v_mfma_f32_16x16x32_bf16 v[52:55], v[188:191], v[68:71], v[52:55]
	s_waitcnt lgkmcnt(11)
	v_mfma_f32_16x16x32_bf16 v[44:47], v[196:199], v[64:67], v[44:47]
	ds_read_b64_tr_b16 v[156:157], v149 offset:49152
	ds_read_b64_tr_b16 v[158:159], v150 offset:49152
	ds_read_b64_tr_b16 v[194:195], v150 offset:57344
	ds_read_b64_tr_b16 v[192:193], v149 offset:57344
	v_mfma_f32_16x16x32_bf16 v[44:47], v[204:207], v[68:71], v[44:47]
	s_waitcnt lgkmcnt(11)
	v_mfma_f32_16x16x32_bf16 v[56:59], v[208:211], v[64:67], v[56:59]
	ds_read_b64_tr_b16 v[200:201], v151 offset:49152
	ds_read_b64_tr_b16 v[202:203], v152 offset:49152
	ds_read_b64_tr_b16 v[190:191], v152 offset:57344
	ds_read_b64_tr_b16 v[188:189], v151 offset:57344
	v_mfma_f32_16x16x32_bf16 v[56:59], v[216:219], v[68:71], v[56:59]
	s_waitcnt lgkmcnt(11)
	v_mfma_f32_16x16x32_bf16 v[48:51], v[224:227], v[64:67], v[48:51]
	v_mfma_f32_16x16x32_bf16 v[48:51], v[88:91], v[68:71], v[48:51]
	s_waitcnt lgkmcnt(7)
	v_mfma_f32_16x16x32_bf16 v[40:43], v[212:215], v[64:67], v[40:43]
	v_mfma_f32_16x16x32_bf16 v[40:43], v[220:223], v[68:71], v[40:43]
	s_waitcnt lgkmcnt(3)
	v_mfma_f32_16x16x32_bf16 v[32:35], v[156:159], v[64:67], v[32:35]
	v_mfma_f32_16x16x32_bf16 v[32:35], v[192:195], v[68:71], v[32:35]
	v_mfma_f32_16x16x32_bf16 v[80:83], v[228:231], v[8:11], v[80:83]
	s_waitcnt lgkmcnt(0)
	v_mfma_f32_16x16x32_bf16 v[36:39], v[200:203], v[64:67], v[36:39]
	v_mfma_f32_16x16x32_bf16 v[80:83], v[92:95], v[12:15], v[80:83]
	v_mfma_f32_16x16x32_bf16 v[36:39], v[188:191], v[68:71], v[36:39]
	s_cbranch_vccnz .LBB0_744
	s_waitcnt vmcnt(3)
	ds_write_b128 v98, v[16:19] offset:16384
	s_waitcnt vmcnt(2)
	ds_write_b128 v99, v[20:23] offset:16384
	s_waitcnt vmcnt(1)
	ds_write_b128 v100, v[24:27] offset:32768
	s_waitcnt vmcnt(0)
	ds_write_b128 v124, v[28:31] offset:32768

.LBB0_766:
	ds_read_b128 v[176:179], v128 offset:16384
	ds_read_b128 v[180:183], v128 offset:17408
	ds_read_b128 v[188:191], v129 offset:16384
	ds_read_b128 v[192:195], v130 offset:16384
	ds_read_b128 v[196:199], v131 offset:16384
	ds_read_b128 v[200:203], v129 offset:17408
	ds_read_b128 v[204:207], v130 offset:17408
	ds_read_b128 v[208:211], v129 offset:24576
	ds_read_b128 v[212:215], v131 offset:17408
	ds_read_b128 v[216:219], v128 offset:24576
	ds_read_b128 v[220:223], v130 offset:24576
	ds_read_b128 v[224:227], v128 offset:25600
	ds_read_b128 v[228:231], v131 offset:24576
	v_pk_mul_f32 v[184:185], v[66:67], v[68:69]
	s_waitcnt lgkmcnt(9)
	v_mfma_f32_16x16x32_bf16 v[160:163], v[176:179], v[0:3], 0
	ds_read_b128 v[176:179], v129 offset:25600
	v_mul_f32_e32 v70, v70, v71
	v_mul_f32_e32 v157, v70, v157
	v_mul_f32_e32 v159, v157, v159
	v_mfma_f32_16x16x32_bf16 v[164:167], v[180:183], v[0:3], 0
	ds_read_b128 v[180:183], v130 offset:25600
	v_mul_f32_e32 v186, v153, v159
	v_pk_mul_f32 v[64:65], v[64:65], v[96:97]
	v_pk_mul_f32 v[72:73], v[72:73], v[74:75]
	v_mfma_f32_16x16x32_bf16 v[160:163], v[188:191], v[4:7], v[160:163]
	ds_read_b128 v[188:191], v131 offset:25600
	v_pk_mul_f32 v[96:97], v[64:65], v[186:187] op_sel_hi:[1,0]
	v_pk_mul_f32 v[84:85], v[84:85], v[94:95]
	v_mfma_f32_16x16x32_bf16 v[66:69], v[192:195], v[8:11], v[160:163]
	ds_read_b64_tr_b16 v[192:193], v142 offset:32768
	ds_read_b64_tr_b16 v[194:195], v143 offset:32768
	v_cvt_pk_bf16_f32 v173, v96, v97
	v_pk_mul_f32 v[96:97], v[76:77], v[78:79]
	s_waitcnt lgkmcnt(10)
	v_mfma_f32_16x16x32_bf16 v[68:71], v[196:199], v[12:15], v[66:69]
	ds_read_b64_tr_b16 v[198:199], v143 offset:40960
	ds_read_b64_tr_b16 v[196:197], v142 offset:40960
	v_pk_mul_f32 v[96:97], v[96:97], v[186:187] op_sel_hi:[1,0]
	v_pk_mul_f32 v[86:87], v[86:87], v[92:93]
	v_mfma_f32_16x16x32_bf16 v[164:167], v[200:203], v[4:7], v[164:167]
	ds_read_b64_tr_b16 v[200:201], v136 offset:32768
	ds_read_b64_tr_b16 v[202:203], v139 offset:32768
	v_mul_f32_e64 v66, v184, v186
	v_mul_f32_e64 v67, v185, v186
	v_pk_mul_f32 v[80:81], v[80:81], v[82:83]
	v_cvt_pk_bf16_f32 v172, v66, v67
	v_mfma_f32_16x16x32_bf16 v[64:67], v[204:207], v[8:11], v[164:167]
	ds_read_b64_tr_b16 v[206:207], v139 offset:40960
	s_and_b64 vcc, exec, s[10:11]
	s_waitcnt lgkmcnt(11)
	v_mfma_f32_16x16x32_bf16 v[64:67], v[212:215], v[12:15], v[64:67]
	ds_read_b64_tr_b16 v[204:205], v136 offset:40960
	ds_read_b64_tr_b16 v[212:213], v138 offset:32768
	ds_read_b64_tr_b16 v[214:215], v141 offset:32768
	v_mfma_f32_16x16x32_bf16 v[168:171], v[216:219], v[0:3], 0
	ds_read_b64_tr_b16 v[218:219], v141 offset:40960
	v_cvt_pk_bf16_f32 v174, v96, v97
	v_pk_mul_f32 v[96:97], v[72:73], v[186:187] op_sel_hi:[1,0]
	v_mfma_f32_16x16x32_bf16 v[76:79], v[208:211], v[4:7], v[168:171]
	v_cvt_pk_bf16_f32 v175, v96, v97
	v_mfma_f32_16x16x32_bf16 v[94:97], v[224:227], v[0:3], 0
	v_mfma_f32_16x16x32_bf16 v[72:75], v[220:223], v[8:11], v[76:79]
	v_mul_f32_e32 v162, v153, v158
	v_pk_mul_f32 v[84:85], v[84:85], v[162:163] op_sel_hi:[1,0]
	v_pk_mul_f32 v[86:87], v[86:87], v[162:163] op_sel_hi:[1,0]
	s_waitcnt lgkmcnt(10)
	v_mfma_f32_16x16x32_bf16 v[92:95], v[176:179], v[4:7], v[94:97]
	ds_read_b64_tr_b16 v[216:217], v138 offset:40960
	ds_read_b64_tr_b16 v[208:209], v137 offset:32768
	ds_read_b64_tr_b16 v[210:211], v140 offset:32768
	ds_read_b64_tr_b16 v[226:227], v140 offset:40960
	ds_read_b64_tr_b16 v[224:225], v137 offset:40960
	v_cvt_pk_bf16_f32 v84, v84, v85
	v_cvt_pk_bf16_f32 v85, v86, v87
	v_pk_mul_f32 v[86:87], v[88:89], v[90:91]
	v_mfma_f32_16x16x32_bf16 v[92:95], v[180:183], v[8:11], v[92:95]
	v_pk_mul_f32 v[86:87], v[86:87], v[162:163] op_sel_hi:[1,0]
	v_mfma_f32_16x16x32_bf16 v[76:79], v[188:191], v[12:15], v[92:95]
	v_cvt_pk_bf16_f32 v86, v86, v87
	s_nop 4
	v_pk_mul_f32 v[92:93], v[80:81], v[162:163] op_sel_hi:[1,0]
	s_waitcnt lgkmcnt(11)
	v_mfma_f32_16x16x32_bf16 v[60:63], v[192:195], v[172:175], v[60:63]
	ds_read_b64_tr_b16 v[220:221], v145 offset:32768
	ds_read_b64_tr_b16 v[222:223], v146 offset:32768
	ds_read_b64_tr_b16 v[178:179], v146 offset:40960
	ds_read_b64_tr_b16 v[176:177], v145 offset:40960
	v_cvt_pk_bf16_f32 v87, v92, v93
	s_waitcnt lgkmcnt(11)
	v_mfma_f32_16x16x32_bf16 v[52:55], v[200:203], v[172:175], v[52:55]
	ds_read_b64_tr_b16 v[180:181], v147 offset:32768
	ds_read_b64_tr_b16 v[182:183], v148 offset:32768
	ds_read_b64_tr_b16 v[190:191], v148 offset:40960
	ds_read_b64_tr_b16 v[188:189], v147 offset:40960
	v_mfma_f32_16x16x32_bf16 v[52:55], v[204:207], v[84:87], v[52:55]
	s_waitcnt lgkmcnt(11)
	v_mfma_f32_16x16x32_bf16 v[44:47], v[212:215], v[172:175], v[44:47]
	ds_read_b64_tr_b16 v[192:193], v149 offset:32768
	ds_read_b64_tr_b16 v[194:195], v150 offset:32768
	ds_read_b64_tr_b16 v[202:203], v150 offset:40960
	ds_read_b64_tr_b16 v[200:201], v149 offset:40960
	v_mfma_f32_16x16x32_bf16 v[44:47], v[216:219], v[84:87], v[44:47]
	s_waitcnt lgkmcnt(11)
	v_mfma_f32_16x16x32_bf16 v[56:59], v[208:211], v[172:175], v[56:59]
	ds_read_b64_tr_b16 v[204:205], v151 offset:32768
	ds_read_b64_tr_b16 v[206:207], v152 offset:32768
	ds_read_b64_tr_b16 v[214:215], v152 offset:40960
	ds_read_b64_tr_b16 v[212:213], v151 offset:40960
	v_mfma_f32_16x16x32_bf16 v[56:59], v[224:227], v[84:87], v[56:59]
	s_waitcnt lgkmcnt(11)
	v_mfma_f32_16x16x32_bf16 v[48:51], v[220:223], v[172:175], v[48:51]
	v_mfma_f32_16x16x32_bf16 v[48:51], v[176:179], v[84:87], v[48:51]
	s_waitcnt lgkmcnt(7)
	v_mfma_f32_16x16x32_bf16 v[40:43], v[180:183], v[172:175], v[40:43]
	v_mfma_f32_16x16x32_bf16 v[40:43], v[188:191], v[84:87], v[40:43]
	s_waitcnt lgkmcnt(3)
	v_mfma_f32_16x16x32_bf16 v[32:35], v[192:195], v[172:175], v[32:35]
	v_mfma_f32_16x16x32_bf16 v[32:35], v[200:203], v[84:87], v[32:35]
	s_waitcnt lgkmcnt(0)
	v_mfma_f32_16x16x32_bf16 v[36:39], v[204:207], v[172:175], v[36:39]
	v_mfma_f32_16x16x32_bf16 v[72:75], v[228:231], v[12:15], v[72:75]
	v_mfma_f32_16x16x32_bf16 v[60:63], v[196:199], v[84:87], v[60:63]
	v_mfma_f32_16x16x32_bf16 v[36:39], v[212:215], v[84:87], v[36:39]
	s_cbranch_vccnz .LBB0_768
	s_waitcnt vmcnt(3)
	ds_write_b128 v98, v[16:19]
	s_waitcnt vmcnt(2)
	ds_write_b128 v99, v[20:23]
	s_waitcnt vmcnt(1)
	ds_write_b128 v100, v[24:27] offset:49152
	s_waitcnt vmcnt(0)
	ds_write_b128 v124, v[28:31] offset:49152

.LBB0_1919:
	ds_read_b128 v[88:91], v129
	ds_read_b128 v[92:95], v129 offset:1024
	ds_read_b128 v[96:99], v130
	ds_read_b128 v[152:155], v130 offset:1024
	ds_read_b128 v[176:179], v131
	ds_read_b128 v[180:183], v131 offset:1024
	ds_read_b128 v[184:187], v132
	ds_read_b128 v[188:191], v132 offset:1024
	ds_read_b128 v[192:195], v129 offset:8192
	ds_read_b128 v[196:199], v129 offset:9216
	ds_read_b128 v[200:203], v130 offset:8192
	ds_read_b128 v[204:207], v130 offset:9216
	ds_read_b128 v[208:211], v131 offset:8192
	ds_read_b128 v[212:215], v131 offset:9216
	ds_read_b128 v[216:219], v132 offset:8192
	s_and_b64 vcc, exec, s[6:7]
	s_waitcnt lgkmcnt(11)
	v_mfma_f32_16x16x32_bf16 v[72:75], v[88:91], v[0:3], 0
	ds_read_b128 v[220:223], v132 offset:9216
	ds_read_b64_tr_b16 v[224:225], v142 offset:49152
	ds_read_b64_tr_b16 v[226:227], v146 offset:49152
	ds_read_b64_tr_b16 v[230:231], v146 offset:57344
	v_mfma_f32_16x16x32_bf16 v[72:75], v[96:99], v[4:7], v[72:75]
	v_mfma_f32_16x16x32_bf16 v[76:79], v[92:95], v[0:3], 0
	s_waitcnt lgkmcnt(11)
	v_mfma_f32_16x16x32_bf16 v[72:75], v[176:179], v[8:11], v[72:75]
	ds_read_b64_tr_b16 v[228:229], v142 offset:57344
	ds_read_b64_tr_b16 v[88:89], v136 offset:49152
	ds_read_b64_tr_b16 v[90:91], v137 offset:49152
	ds_read_b64_tr_b16 v[98:99], v137 offset:57344
	v_mfma_f32_16x16x32_bf16 v[84:87], v[184:187], v[12:15], v[72:75]
	v_mfma_f32_16x16x32_bf16 v[72:75], v[152:155], v[4:7], v[76:79]
	v_mfma_f32_16x16x32_bf16 v[72:75], v[180:183], v[8:11], v[72:75]
	v_mfma_f32_16x16x32_bf16 v[80:83], v[188:191], v[12:15], v[72:75]
	s_waitcnt lgkmcnt(11)
	s_nop 5
	v_mfma_f32_16x16x32_bf16 v[72:75], v[192:195], v[0:3], 0
	ds_read_b64_tr_b16 v[96:97], v136 offset:57344
	ds_read_b64_tr_b16 v[92:93], v139 offset:49152
	ds_read_b64_tr_b16 v[94:95], v145 offset:49152
	ds_read_b64_tr_b16 v[178:179], v145 offset:57344
	v_mfma_f32_16x16x32_bf16 v[72:75], v[200:203], v[4:7], v[72:75]
	s_waitcnt lgkmcnt(11)
	v_mfma_f32_16x16x32_bf16 v[72:75], v[208:211], v[8:11], v[72:75]
	ds_read_b64_tr_b16 v[176:177], v139 offset:57344
	ds_read_b64_tr_b16 v[184:185], v140 offset:49152
	ds_read_b64_tr_b16 v[186:187], v147 offset:49152
	ds_read_b64_tr_b16 v[154:155], v147 offset:57344
	v_mfma_f32_16x16x32_bf16 v[76:79], v[216:219], v[12:15], v[72:75]
	v_mfma_f32_16x16x32_bf16 v[72:75], v[196:199], v[0:3], 0
	v_mfma_f32_16x16x32_bf16 v[72:75], v[204:207], v[4:7], v[72:75]
	s_waitcnt lgkmcnt(10)
	v_mfma_f32_16x16x32_bf16 v[60:63], v[224:227], v[68:71], v[60:63]
	ds_read_b64_tr_b16 v[152:153], v140 offset:57344
	ds_read_b64_tr_b16 v[180:181], v148 offset:49152
	ds_read_b64_tr_b16 v[182:183], v149 offset:49152
	ds_read_b64_tr_b16 v[190:191], v149 offset:57344
	ds_read_b64_tr_b16 v[188:189], v148 offset:57344
	v_mfma_f32_16x16x32_bf16 v[60:63], v[228:231], v[64:67], v[60:63]
	s_waitcnt lgkmcnt(11)
	v_mfma_f32_16x16x32_bf16 v[52:55], v[88:91], v[68:71], v[52:55]
	ds_read_b64_tr_b16 v[192:193], v133 offset:49152
	ds_read_b64_tr_b16 v[194:195], v134 offset:49152
	ds_read_b64_tr_b16 v[202:203], v134 offset:57344
	ds_read_b64_tr_b16 v[200:201], v133 offset:57344
	v_mfma_f32_16x16x32_bf16 v[52:55], v[96:99], v[64:67], v[52:55]
	s_waitcnt lgkmcnt(11)
	v_mfma_f32_16x16x32_bf16 v[48:51], v[92:95], v[68:71], v[48:51]
	ds_read_b64_tr_b16 v[208:209], v135 offset:49152
	ds_read_b64_tr_b16 v[210:211], v138 offset:49152
	ds_read_b64_tr_b16 v[218:219], v138 offset:57344
	ds_read_b64_tr_b16 v[216:217], v135 offset:57344
	v_mfma_f32_16x16x32_bf16 v[48:51], v[176:179], v[64:67], v[48:51]
	s_waitcnt lgkmcnt(11)
	v_mfma_f32_16x16x32_bf16 v[56:59], v[184:187], v[68:71], v[56:59]
	ds_read_b64_tr_b16 v[196:197], v141 offset:49152
	ds_read_b64_tr_b16 v[198:199], v143 offset:49152
	ds_read_b64_tr_b16 v[206:207], v143 offset:57344
	ds_read_b64_tr_b16 v[204:205], v141 offset:57344
	v_mfma_f32_16x16x32_bf16 v[56:59], v[152:155], v[64:67], v[56:59]
	s_waitcnt lgkmcnt(11)
	v_mfma_f32_16x16x32_bf16 v[32:35], v[180:183], v[68:71], v[32:35]
	v_mfma_f32_16x16x32_bf16 v[32:35], v[188:191], v[64:67], v[32:35]
	s_waitcnt lgkmcnt(7)
	v_mfma_f32_16x16x32_bf16 v[36:39], v[192:195], v[68:71], v[36:39]
	v_mfma_f32_16x16x32_bf16 v[36:39], v[200:203], v[64:67], v[36:39]
	s_waitcnt lgkmcnt(3)
	v_mfma_f32_16x16x32_bf16 v[40:43], v[208:211], v[68:71], v[40:43]
	v_mfma_f32_16x16x32_bf16 v[40:43], v[216:219], v[64:67], v[40:43]
	v_mfma_f32_16x16x32_bf16 v[72:75], v[212:215], v[8:11], v[72:75]
	s_waitcnt lgkmcnt(0)
	v_mfma_f32_16x16x32_bf16 v[44:47], v[196:199], v[68:71], v[44:47]
	v_mfma_f32_16x16x32_bf16 v[72:75], v[220:223], v[12:15], v[72:75]
	v_mfma_f32_16x16x32_bf16 v[44:47], v[204:207], v[64:67], v[44:47]
	s_cbranch_vccnz .LBB0_1921
	v_add_u32_e32 v64, 0, v109
	s_waitcnt vmcnt(3)
	ds_write_b128 v100, v[16:19] offset:16384
	s_waitcnt vmcnt(2)
	ds_write_b128 v124, v[20:23] offset:16384
	s_waitcnt vmcnt(1)
	ds_write_b128 v64, v[24:27] offset:32768
	v_add_u32_e32 v64, 0, v112
	s_waitcnt vmcnt(0)
	ds_write_b128 v64, v[28:31] offset:32768

.LBB0_1927:
	ds_read_b128 v[168:171], v129 offset:16384
	ds_read_b128 v[172:175], v130 offset:16384
	ds_read_b128 v[176:179], v131 offset:16384
	ds_read_b128 v[180:183], v129 offset:17408
	ds_read_b128 v[184:187], v132 offset:16384
	ds_read_b128 v[188:191], v130 offset:17408
	ds_read_b128 v[192:195], v131 offset:17408
	ds_read_b128 v[196:199], v129 offset:24576
	ds_read_b128 v[200:203], v132 offset:17408
	ds_read_b128 v[204:207], v130 offset:24576
	ds_read_b128 v[208:211], v131 offset:24576
	ds_read_b128 v[212:215], v129 offset:25600
	ds_read_b128 v[216:219], v132 offset:24576
	ds_read_b128 v[220:223], v130 offset:25600
	ds_read_b128 v[224:227], v131 offset:25600
	v_sub_f32_e32 v64, v127, v96
	v_add_f32_e32 v64, v84, v64
	v_exp_f32_e32 v96, v64
	v_sub_f32_e32 v64, v127, v97
	v_add_f32_e32 v64, v85, v64
	v_exp_f32_e32 v97, v64
	v_sub_f32_e32 v64, v127, v98
	v_add_f32_e32 v64, v86, v64
	v_exp_f32_e32 v98, v64
	v_sub_f32_e32 v64, v127, v99
	v_add_f32_e32 v64, v87, v64
	v_exp_f32_e32 v99, v64
	v_sub_f32_e32 v64, v127, v92
	v_add_f32_e32 v64, v80, v64
	v_exp_f32_e32 v153, v64
	v_sub_f32_e32 v64, v127, v93
	v_add_f32_e32 v64, v81, v64
	v_exp_f32_e32 v154, v64
	v_sub_f32_e32 v64, v127, v94
	v_add_f32_e32 v64, v82, v64
	v_exp_f32_e32 v155, v64
	v_sub_f32_e32 v64, v127, v95
	v_add_f32_e32 v64, v83, v64
	s_waitcnt lgkmcnt(11)
	v_mfma_f32_16x16x32_bf16 v[84:87], v[168:171], v[0:3], 0
	ds_read_b128 v[228:231], v132 offset:25600
	ds_read_b64_tr_b16 v[168:169], v142 offset:32768
	ds_read_b64_tr_b16 v[170:171], v146 offset:32768
	v_exp_f32_e32 v156, v64
	v_sub_f32_e32 v64, v127, v88
	v_add_f32_e32 v64, v76, v64
	v_exp_f32_e32 v157, v64
	v_sub_f32_e32 v64, v127, v89
	v_mfma_f32_16x16x32_bf16 v[92:95], v[180:183], v[0:3], 0
	ds_read_b64_tr_b16 v[182:183], v146 offset:40960
	v_add_f32_e32 v64, v77, v64
	v_sub_f32_e32 v70, v127, v67
	v_add_f32_e32 v70, v73, v70
	v_mfma_f32_16x16x32_bf16 v[84:87], v[172:175], v[4:7], v[84:87]
	v_exp_f32_e32 v158, v64
	v_sub_f32_e32 v64, v127, v90
	v_add_f32_e32 v64, v78, v64
	v_exp_f32_e32 v159, v64
	v_sub_f32_e32 v64, v127, v91
	s_waitcnt lgkmcnt(10)
	v_mfma_f32_16x16x32_bf16 v[88:91], v[188:191], v[4:7], v[92:95]
	ds_read_b64_tr_b16 v[180:181], v142 offset:40960
	ds_read_b64_tr_b16 v[172:173], v136 offset:32768
	ds_read_b64_tr_b16 v[174:175], v137 offset:32768
	ds_read_b64_tr_b16 v[190:191], v137 offset:40960
	ds_read_b64_tr_b16 v[188:189], v136 offset:40960
	v_add_f32_e32 v64, v79, v64
	v_exp_f32_e32 v160, v64
	v_sub_f32_e32 v64, v127, v66
	v_mfma_f32_16x16x32_bf16 v[80:83], v[176:179], v[8:11], v[84:87]
	v_add_f32_e32 v64, v72, v64
	v_exp_f32_e32 v161, v64
	v_sub_f32_e32 v68, v127, v68
	v_mfma_f32_16x16x32_bf16 v[76:79], v[192:195], v[8:11], v[88:91]
	v_add_f32_e32 v68, v74, v68
	s_and_b64 vcc, exec, s[6:7]
	v_mfma_f32_16x16x32_bf16 v[92:95], v[196:199], v[0:3], 0
	v_mfma_f32_16x16x32_bf16 v[80:83], v[184:187], v[12:15], v[80:83]
	v_exp_f32_e32 v162, v70
	v_exp_f32_e32 v163, v68
	v_sub_f32_e32 v68, v127, v69
	v_mfma_f32_16x16x32_bf16 v[76:79], v[200:203], v[12:15], v[76:79]
	s_waitcnt lgkmcnt(11)
	v_mfma_f32_16x16x32_bf16 v[88:91], v[204:207], v[4:7], v[92:95]
	ds_read_b64_tr_b16 v[176:177], v139 offset:32768
	ds_read_b64_tr_b16 v[178:179], v145 offset:32768
	ds_read_b64_tr_b16 v[194:195], v145 offset:40960
	ds_read_b64_tr_b16 v[192:193], v139 offset:40960
	v_add_f32_e32 v68, v75, v68
	v_mfma_f32_16x16x32_bf16 v[84:87], v[208:211], v[8:11], v[88:91]
	v_cvt_pk_bf16_f32 v92, v96, v97
	v_cvt_pk_bf16_f32 v93, v98, v99
	v_cvt_pk_bf16_f32 v94, v153, v154
	v_mfma_f32_16x16x32_bf16 v[64:67], v[216:219], v[12:15], v[84:87]
	v_cvt_pk_bf16_f32 v95, v155, v156
	v_mfma_f32_16x16x32_bf16 v[84:87], v[212:215], v[0:3], 0
	v_exp_f32_e32 v164, v68
	s_waitcnt lgkmcnt(11)
	v_mfma_f32_16x16x32_bf16 v[84:87], v[220:223], v[4:7], v[84:87]
	ds_read_b64_tr_b16 v[196:197], v140 offset:32768
	ds_read_b64_tr_b16 v[198:199], v147 offset:32768
	ds_read_b64_tr_b16 v[186:187], v147 offset:40960
	ds_read_b64_tr_b16 v[184:185], v140 offset:40960
	v_mfma_f32_16x16x32_bf16 v[68:71], v[224:227], v[8:11], v[84:87]
	s_nop 2
	v_cvt_pk_bf16_f32 v84, v157, v158
	v_mfma_f32_16x16x32_bf16 v[68:71], v[228:231], v[12:15], v[68:71]
	v_cvt_pk_bf16_f32 v85, v159, v160
	v_cvt_pk_bf16_f32 v86, v161, v162
	s_waitcnt lgkmcnt(11)
	v_mfma_f32_16x16x32_bf16 v[60:63], v[168:171], v[92:95], v[60:63]
	ds_read_b64_tr_b16 v[200:201], v148 offset:32768
	ds_read_b64_tr_b16 v[202:203], v149 offset:32768
	ds_read_b64_tr_b16 v[206:207], v149 offset:40960
	ds_read_b64_tr_b16 v[204:205], v148 offset:40960
	v_cvt_pk_bf16_f32 v87, v163, v164
	s_nop 1
	v_mfma_f32_16x16x32_bf16 v[60:63], v[180:183], v[84:87], v[60:63]
	s_waitcnt lgkmcnt(11)
	v_mfma_f32_16x16x32_bf16 v[52:55], v[172:175], v[92:95], v[52:55]
	ds_read_b64_tr_b16 v[208:209], v133 offset:32768
	ds_read_b64_tr_b16 v[210:211], v134 offset:32768
	ds_read_b64_tr_b16 v[218:219], v134 offset:40960
	ds_read_b64_tr_b16 v[216:217], v133 offset:40960
	v_mfma_f32_16x16x32_bf16 v[52:55], v[188:191], v[84:87], v[52:55]
	s_waitcnt lgkmcnt(11)
	v_mfma_f32_16x16x32_bf16 v[48:51], v[176:179], v[92:95], v[48:51]
	ds_read_b64_tr_b16 v[212:213], v135 offset:32768
	ds_read_b64_tr_b16 v[214:215], v138 offset:32768
	ds_read_b64_tr_b16 v[222:223], v138 offset:40960
	ds_read_b64_tr_b16 v[220:221], v135 offset:40960
	v_mfma_f32_16x16x32_bf16 v[48:51], v[192:195], v[84:87], v[48:51]
	s_waitcnt lgkmcnt(11)
	v_mfma_f32_16x16x32_bf16 v[56:59], v[196:199], v[92:95], v[56:59]
	ds_read_b64_tr_b16 v[224:225], v141 offset:32768
	ds_read_b64_tr_b16 v[226:227], v143 offset:32768
	ds_read_b64_tr_b16 v[230:231], v143 offset:40960
	ds_read_b64_tr_b16 v[228:229], v141 offset:40960
	v_mfma_f32_16x16x32_bf16 v[56:59], v[184:187], v[84:87], v[56:59]
	s_waitcnt lgkmcnt(11)
	v_mfma_f32_16x16x32_bf16 v[32:35], v[200:203], v[92:95], v[32:35]
	v_mfma_f32_16x16x32_bf16 v[32:35], v[204:207], v[84:87], v[32:35]
	s_waitcnt lgkmcnt(7)
	v_mfma_f32_16x16x32_bf16 v[36:39], v[208:211], v[92:95], v[36:39]
	v_mfma_f32_16x16x32_bf16 v[36:39], v[216:219], v[84:87], v[36:39]
	s_waitcnt lgkmcnt(3)
	v_mfma_f32_16x16x32_bf16 v[40:43], v[212:215], v[92:95], v[40:43]
	v_mfma_f32_16x16x32_bf16 v[40:43], v[220:223], v[84:87], v[40:43]
	s_waitcnt lgkmcnt(0)
	v_mfma_f32_16x16x32_bf16 v[44:47], v[224:227], v[92:95], v[44:47]
	v_mfma_f32_16x16x32_bf16 v[44:47], v[228:231], v[84:87], v[44:47]
	s_cbranch_vccnz .LBB0_1929
	v_add_u32_e32 v72, 0, v109
	s_waitcnt vmcnt(3)
	ds_write_b128 v100, v[16:19]
	s_waitcnt vmcnt(2)
	ds_write_b128 v124, v[20:23]
	s_waitcnt vmcnt(1)
	ds_write_b128 v72, v[24:27] offset:49152
	v_add_u32_e32 v72, 0, v112
	s_waitcnt vmcnt(0)
	ds_write_b128 v72, v[28:31] offset:49152

.LBB0_1958:
	ds_read_b128 v[88:91], v129
	ds_read_b128 v[92:95], v129 offset:1024
	ds_read_b128 v[96:99], v130
	ds_read_b128 v[152:155], v130 offset:1024
	ds_read_b128 v[172:175], v131
	ds_read_b128 v[176:179], v131 offset:1024
	ds_read_b128 v[180:183], v132
	ds_read_b128 v[184:187], v132 offset:1024
	ds_read_b128 v[188:191], v129 offset:8192
	ds_read_b128 v[192:195], v129 offset:9216
	ds_read_b128 v[196:199], v130 offset:8192
	ds_read_b128 v[200:203], v130 offset:9216
	ds_read_b128 v[204:207], v131 offset:8192
	ds_read_b128 v[208:211], v131 offset:9216
	ds_read_b128 v[212:215], v132 offset:8192
	s_and_b64 vcc, exec, s[6:7]
	s_waitcnt lgkmcnt(11)
	v_mfma_f32_16x16x32_bf16 v[72:75], v[88:91], v[0:3], 0
	ds_read_b128 v[216:219], v132 offset:9216
	ds_read_b64_tr_b16 v[220:221], v146 offset:49152
	ds_read_b64_tr_b16 v[222:223], v148 offset:49152
	ds_read_b64_tr_b16 v[226:227], v148 offset:57344
	v_mfma_f32_16x16x32_bf16 v[72:75], v[96:99], v[4:7], v[72:75]
	v_mfma_f32_16x16x32_bf16 v[76:79], v[92:95], v[0:3], 0
	s_waitcnt lgkmcnt(11)
	v_mfma_f32_16x16x32_bf16 v[72:75], v[172:175], v[8:11], v[72:75]
	ds_read_b64_tr_b16 v[224:225], v146 offset:57344
	ds_read_b64_tr_b16 v[228:229], v139 offset:49152
	ds_read_b64_tr_b16 v[230:231], v142 offset:49152
	ds_read_b64_tr_b16 v[90:91], v142 offset:57344
	v_mfma_f32_16x16x32_bf16 v[84:87], v[180:183], v[12:15], v[72:75]
	v_mfma_f32_16x16x32_bf16 v[72:75], v[152:155], v[4:7], v[76:79]
	v_mfma_f32_16x16x32_bf16 v[72:75], v[176:179], v[8:11], v[72:75]
	v_mfma_f32_16x16x32_bf16 v[80:83], v[184:187], v[12:15], v[72:75]
	s_waitcnt lgkmcnt(11)
	s_nop 5
	v_mfma_f32_16x16x32_bf16 v[72:75], v[188:191], v[0:3], 0
	ds_read_b64_tr_b16 v[88:89], v139 offset:57344
	ds_read_b64_tr_b16 v[96:97], v141 offset:49152
	ds_read_b64_tr_b16 v[98:99], v145 offset:49152
	ds_read_b64_tr_b16 v[94:95], v145 offset:57344
	v_mfma_f32_16x16x32_bf16 v[72:75], v[196:199], v[4:7], v[72:75]
	s_waitcnt lgkmcnt(11)
	v_mfma_f32_16x16x32_bf16 v[72:75], v[204:207], v[8:11], v[72:75]
	ds_read_b64_tr_b16 v[92:93], v141 offset:57344
	ds_read_b64_tr_b16 v[172:173], v140 offset:49152
	ds_read_b64_tr_b16 v[174:175], v143 offset:49152
	ds_read_b64_tr_b16 v[182:183], v143 offset:57344
	v_mfma_f32_16x16x32_bf16 v[76:79], v[212:215], v[12:15], v[72:75]
	v_mfma_f32_16x16x32_bf16 v[72:75], v[192:195], v[0:3], 0
	v_mfma_f32_16x16x32_bf16 v[72:75], v[200:203], v[4:7], v[72:75]
	s_waitcnt lgkmcnt(10)
	v_mfma_f32_16x16x32_bf16 v[60:63], v[220:223], v[68:71], v[60:63]
	ds_read_b64_tr_b16 v[180:181], v140 offset:57344
	ds_read_b64_tr_b16 v[152:153], v147 offset:49152
	ds_read_b64_tr_b16 v[154:155], v149 offset:49152
	ds_read_b64_tr_b16 v[178:179], v149 offset:57344
	ds_read_b64_tr_b16 v[176:177], v147 offset:57344
	v_mfma_f32_16x16x32_bf16 v[60:63], v[224:227], v[64:67], v[60:63]
	s_waitcnt lgkmcnt(11)
	v_mfma_f32_16x16x32_bf16 v[56:59], v[228:231], v[68:71], v[56:59]
	ds_read_b64_tr_b16 v[184:185], v133 offset:49152
	ds_read_b64_tr_b16 v[186:187], v134 offset:49152
	ds_read_b64_tr_b16 v[190:191], v134 offset:57344
	ds_read_b64_tr_b16 v[188:189], v133 offset:57344
	v_mfma_f32_16x16x32_bf16 v[56:59], v[88:91], v[64:67], v[56:59]
	s_waitcnt lgkmcnt(11)
	v_mfma_f32_16x16x32_bf16 v[52:55], v[96:99], v[68:71], v[52:55]
	ds_read_b64_tr_b16 v[196:197], v135 offset:49152
	ds_read_b64_tr_b16 v[198:199], v136 offset:49152
	ds_read_b64_tr_b16 v[206:207], v136 offset:57344
	ds_read_b64_tr_b16 v[204:205], v135 offset:57344
	v_mfma_f32_16x16x32_bf16 v[52:55], v[92:95], v[64:67], v[52:55]
	s_waitcnt lgkmcnt(11)
	v_mfma_f32_16x16x32_bf16 v[48:51], v[172:175], v[68:71], v[48:51]
	ds_read_b64_tr_b16 v[212:213], v137 offset:49152
	ds_read_b64_tr_b16 v[214:215], v138 offset:49152
	ds_read_b64_tr_b16 v[194:195], v138 offset:57344
	ds_read_b64_tr_b16 v[192:193], v137 offset:57344
	v_mfma_f32_16x16x32_bf16 v[48:51], v[180:183], v[64:67], v[48:51]
	s_waitcnt lgkmcnt(11)
	v_mfma_f32_16x16x32_bf16 v[32:35], v[152:155], v[68:71], v[32:35]
	v_mfma_f32_16x16x32_bf16 v[32:35], v[176:179], v[64:67], v[32:35]
	s_waitcnt lgkmcnt(7)
	v_mfma_f32_16x16x32_bf16 v[36:39], v[184:187], v[68:71], v[36:39]
	v_mfma_f32_16x16x32_bf16 v[36:39], v[188:191], v[64:67], v[36:39]
	s_waitcnt lgkmcnt(3)
	v_mfma_f32_16x16x32_bf16 v[40:43], v[196:199], v[68:71], v[40:43]
	v_mfma_f32_16x16x32_bf16 v[40:43], v[204:207], v[64:67], v[40:43]
	v_mfma_f32_16x16x32_bf16 v[72:75], v[208:211], v[8:11], v[72:75]
	s_waitcnt lgkmcnt(0)
	v_mfma_f32_16x16x32_bf16 v[44:47], v[212:215], v[68:71], v[44:47]
	v_mfma_f32_16x16x32_bf16 v[72:75], v[216:219], v[12:15], v[72:75]
	v_mfma_f32_16x16x32_bf16 v[44:47], v[192:195], v[64:67], v[44:47]
	s_cbranch_vccnz .LBB0_1960
	v_add_u32_e32 v64, 0, v109
	s_waitcnt vmcnt(3)
	ds_write_b128 v100, v[16:19] offset:16384
	s_waitcnt vmcnt(2)
	ds_write_b128 v124, v[20:23] offset:16384
	s_waitcnt vmcnt(1)
	ds_write_b128 v64, v[24:27] offset:32768
	v_add_u32_e32 v64, 0, v112
	s_waitcnt vmcnt(0)
	ds_write_b128 v64, v[28:31] offset:32768

.LBB0_1966:
	ds_read_b128 v[164:167], v129 offset:16384
	ds_read_b128 v[168:171], v130 offset:16384
	ds_read_b128 v[172:175], v131 offset:16384
	ds_read_b128 v[176:179], v129 offset:17408
	ds_read_b128 v[180:183], v132 offset:16384
	ds_read_b128 v[184:187], v130 offset:17408
	ds_read_b128 v[188:191], v131 offset:17408
	ds_read_b128 v[192:195], v129 offset:24576
	ds_read_b128 v[196:199], v132 offset:17408
	ds_read_b128 v[200:203], v130 offset:24576
	ds_read_b128 v[204:207], v131 offset:24576
	ds_read_b128 v[208:211], v129 offset:25600
	ds_read_b128 v[212:215], v132 offset:24576
	ds_read_b128 v[216:219], v130 offset:25600
	ds_read_b128 v[220:223], v131 offset:25600
	v_sub_f32_e32 v64, v128, v96
	v_add_f32_e32 v64, v84, v64
	v_exp_f32_e32 v96, v64
	v_sub_f32_e32 v64, v128, v97
	v_add_f32_e32 v64, v85, v64
	v_exp_f32_e32 v97, v64
	v_sub_f32_e32 v64, v128, v98
	v_add_f32_e32 v64, v86, v64
	v_exp_f32_e32 v98, v64
	v_sub_f32_e32 v64, v128, v99
	v_add_f32_e32 v64, v87, v64
	v_exp_f32_e32 v99, v64
	v_sub_f32_e32 v64, v128, v92
	v_add_f32_e32 v64, v80, v64
	v_exp_f32_e32 v152, v64
	v_sub_f32_e32 v64, v128, v93
	v_add_f32_e32 v64, v81, v64
	v_exp_f32_e32 v153, v64
	v_sub_f32_e32 v64, v128, v94
	v_add_f32_e32 v64, v82, v64
	v_exp_f32_e32 v154, v64
	v_sub_f32_e32 v64, v128, v95
	v_add_f32_e32 v64, v83, v64
	s_waitcnt lgkmcnt(11)
	v_mfma_f32_16x16x32_bf16 v[84:87], v[164:167], v[0:3], 0
	ds_read_b128 v[224:227], v132 offset:25600
	ds_read_b64_tr_b16 v[228:229], v146 offset:32768
	ds_read_b64_tr_b16 v[230:231], v148 offset:32768
	ds_read_b64_tr_b16 v[166:167], v148 offset:40960
	v_exp_f32_e32 v155, v64
	v_sub_f32_e32 v64, v128, v88
	v_add_f32_e32 v64, v76, v64
	v_mfma_f32_16x16x32_bf16 v[84:87], v[168:171], v[4:7], v[84:87]
	v_exp_f32_e32 v156, v64
	v_sub_f32_e32 v64, v128, v89
	v_add_f32_e32 v64, v77, v64
	v_mfma_f32_16x16x32_bf16 v[92:95], v[176:179], v[0:3], 0
	v_exp_f32_e32 v157, v64
	v_sub_f32_e32 v64, v128, v90
	v_add_f32_e32 v64, v78, v64
	v_exp_f32_e32 v158, v64
	v_sub_f32_e32 v64, v128, v91
	s_waitcnt lgkmcnt(10)
	v_mfma_f32_16x16x32_bf16 v[88:91], v[184:187], v[4:7], v[92:95]
	ds_read_b64_tr_b16 v[164:165], v146 offset:40960
	ds_read_b64_tr_b16 v[168:169], v139 offset:32768
	ds_read_b64_tr_b16 v[170:171], v142 offset:32768
	ds_read_b64_tr_b16 v[178:179], v142 offset:40960
	ds_read_b64_tr_b16 v[176:177], v139 offset:40960
	v_add_f32_e32 v64, v79, v64
	v_exp_f32_e32 v159, v64
	v_sub_f32_e32 v64, v128, v66
	v_mfma_f32_16x16x32_bf16 v[80:83], v[172:175], v[8:11], v[84:87]
	v_add_f32_e32 v64, v72, v64
	v_sub_f32_e32 v70, v128, v67
	v_add_f32_e32 v70, v73, v70
	v_mfma_f32_16x16x32_bf16 v[76:79], v[188:191], v[8:11], v[88:91]
	v_sub_f32_e32 v68, v128, v68
	v_add_f32_e32 v68, v74, v68
	s_and_b64 vcc, exec, s[6:7]
	v_mfma_f32_16x16x32_bf16 v[92:95], v[192:195], v[0:3], 0
	v_mfma_f32_16x16x32_bf16 v[76:79], v[196:199], v[12:15], v[76:79]
	s_waitcnt lgkmcnt(11)
	v_mfma_f32_16x16x32_bf16 v[88:91], v[200:203], v[4:7], v[92:95]
	ds_read_b64_tr_b16 v[184:185], v141 offset:32768
	ds_read_b64_tr_b16 v[186:187], v145 offset:32768
	ds_read_b64_tr_b16 v[174:175], v145 offset:40960
	ds_read_b64_tr_b16 v[172:173], v141 offset:40960
	v_mfma_f32_16x16x32_bf16 v[80:83], v[180:183], v[12:15], v[80:83]
	v_exp_f32_e32 v160, v64
	v_exp_f32_e32 v161, v70
	v_mfma_f32_16x16x32_bf16 v[84:87], v[204:207], v[8:11], v[88:91]
	v_exp_f32_e32 v162, v68
	v_sub_f32_e32 v68, v128, v69
	v_mfma_f32_16x16x32_bf16 v[64:67], v[212:215], v[12:15], v[84:87]
	v_add_f32_e32 v68, v75, v68
	v_exp_f32_e32 v163, v68
	v_mfma_f32_16x16x32_bf16 v[84:87], v[208:211], v[0:3], 0
	v_cvt_pk_bf16_f32 v92, v96, v97
	v_cvt_pk_bf16_f32 v93, v98, v99
	s_waitcnt lgkmcnt(11)
	v_mfma_f32_16x16x32_bf16 v[84:87], v[216:219], v[4:7], v[84:87]
	ds_read_b64_tr_b16 v[188:189], v140 offset:32768
	ds_read_b64_tr_b16 v[190:191], v143 offset:32768
	ds_read_b64_tr_b16 v[194:195], v143 offset:40960
	ds_read_b64_tr_b16 v[192:193], v140 offset:40960
	v_cvt_pk_bf16_f32 v94, v152, v153
	v_cvt_pk_bf16_f32 v95, v154, v155
	v_mfma_f32_16x16x32_bf16 v[68:71], v[220:223], v[8:11], v[84:87]
	s_nop 2
	v_cvt_pk_bf16_f32 v84, v156, v157
	v_mfma_f32_16x16x32_bf16 v[68:71], v[224:227], v[12:15], v[68:71]
	v_cvt_pk_bf16_f32 v85, v158, v159
	v_cvt_pk_bf16_f32 v86, v160, v161
	s_waitcnt lgkmcnt(11)
	v_mfma_f32_16x16x32_bf16 v[60:63], v[228:231], v[92:95], v[60:63]
	ds_read_b64_tr_b16 v[196:197], v147 offset:32768
	ds_read_b64_tr_b16 v[198:199], v149 offset:32768
	ds_read_b64_tr_b16 v[202:203], v149 offset:40960
	ds_read_b64_tr_b16 v[200:201], v147 offset:40960
	v_cvt_pk_bf16_f32 v87, v162, v163
	s_nop 1
	v_mfma_f32_16x16x32_bf16 v[60:63], v[164:167], v[84:87], v[60:63]
	s_waitcnt lgkmcnt(11)
	v_mfma_f32_16x16x32_bf16 v[56:59], v[168:171], v[92:95], v[56:59]
	ds_read_b64_tr_b16 v[180:181], v133 offset:32768
	ds_read_b64_tr_b16 v[182:183], v134 offset:32768
	ds_read_b64_tr_b16 v[206:207], v134 offset:40960
	ds_read_b64_tr_b16 v[204:205], v133 offset:40960
	v_mfma_f32_16x16x32_bf16 v[56:59], v[176:179], v[84:87], v[56:59]
	s_waitcnt lgkmcnt(11)
	v_mfma_f32_16x16x32_bf16 v[52:55], v[184:187], v[92:95], v[52:55]
	ds_read_b64_tr_b16 v[212:213], v135 offset:32768
	ds_read_b64_tr_b16 v[214:215], v136 offset:32768
	ds_read_b64_tr_b16 v[210:211], v136 offset:40960
	ds_read_b64_tr_b16 v[208:209], v135 offset:40960
	v_mfma_f32_16x16x32_bf16 v[52:55], v[172:175], v[84:87], v[52:55]
	s_waitcnt lgkmcnt(11)
	v_mfma_f32_16x16x32_bf16 v[48:51], v[188:191], v[92:95], v[48:51]
	ds_read_b64_tr_b16 v[216:217], v137 offset:32768
	ds_read_b64_tr_b16 v[218:219], v138 offset:32768
	ds_read_b64_tr_b16 v[222:223], v138 offset:40960
	ds_read_b64_tr_b16 v[220:221], v137 offset:40960
	v_mfma_f32_16x16x32_bf16 v[48:51], v[192:195], v[84:87], v[48:51]
	s_waitcnt lgkmcnt(11)
	v_mfma_f32_16x16x32_bf16 v[32:35], v[196:199], v[92:95], v[32:35]
	v_mfma_f32_16x16x32_bf16 v[32:35], v[200:203], v[84:87], v[32:35]
	s_waitcnt lgkmcnt(7)
	v_mfma_f32_16x16x32_bf16 v[36:39], v[180:183], v[92:95], v[36:39]
	v_mfma_f32_16x16x32_bf16 v[36:39], v[204:207], v[84:87], v[36:39]
	s_waitcnt lgkmcnt(3)
	v_mfma_f32_16x16x32_bf16 v[40:43], v[212:215], v[92:95], v[40:43]
	v_mfma_f32_16x16x32_bf16 v[40:43], v[208:211], v[84:87], v[40:43]
	s_waitcnt lgkmcnt(0)
	v_mfma_f32_16x16x32_bf16 v[44:47], v[216:219], v[92:95], v[44:47]
	v_mfma_f32_16x16x32_bf16 v[44:47], v[220:223], v[84:87], v[44:47]
	s_cbranch_vccnz .LBB0_1968
	v_add_u32_e32 v72, 0, v109
	s_waitcnt vmcnt(3)
	ds_write_b128 v100, v[16:19]
	s_waitcnt vmcnt(2)
	ds_write_b128 v124, v[20:23]
	s_waitcnt vmcnt(1)
	ds_write_b128 v72, v[24:27] offset:49152
	v_add_u32_e32 v72, 0, v112
	s_waitcnt vmcnt(0)
	ds_write_b128 v72, v[28:31] offset:49152

.LBB0_2030:
	ds_read_b128 v[88:91], v128
	ds_read_b128 v[92:95], v128 offset:1024
	ds_read_b128 v[156:159], v129
	ds_read_b128 v[188:191], v129 offset:1024
	ds_read_b128 v[192:195], v130
	ds_read_b128 v[196:199], v130 offset:1024
	ds_read_b128 v[200:203], v131
	ds_read_b128 v[204:207], v131 offset:1024
	ds_read_b128 v[208:211], v128 offset:8192
	ds_read_b128 v[212:215], v128 offset:9216
	ds_read_b128 v[216:219], v129 offset:8192
	ds_read_b128 v[220:223], v129 offset:9216
	ds_read_b128 v[224:227], v130 offset:8192
	ds_read_b128 v[228:231], v130 offset:9216
	s_and_b64 vcc, exec, s[6:7]
	s_waitcnt lgkmcnt(10)
	v_mfma_f32_16x16x32_bf16 v[72:75], v[88:91], v[0:3], 0
	ds_read_b128 v[88:91], v131 offset:8192
	v_mfma_f32_16x16x32_bf16 v[80:83], v[92:95], v[0:3], 0
	ds_read_b128 v[92:95], v131 offset:9216
	v_mfma_f32_16x16x32_bf16 v[72:75], v[156:159], v[4:7], v[72:75]
	ds_read_b64_tr_b16 v[156:157], v140 offset:49152
	ds_read_b64_tr_b16 v[158:159], v141 offset:49152
	s_waitcnt lgkmcnt(10)
	v_mfma_f32_16x16x32_bf16 v[72:75], v[192:195], v[8:11], v[72:75]
	ds_read_b64_tr_b16 v[194:195], v141 offset:57344
	ds_read_b64_tr_b16 v[192:193], v140 offset:57344
	v_mfma_f32_16x16x32_bf16 v[76:79], v[200:203], v[12:15], v[72:75]
	ds_read_b64_tr_b16 v[200:201], v136 offset:49152
	ds_read_b64_tr_b16 v[202:203], v137 offset:49152
	v_mfma_f32_16x16x32_bf16 v[72:75], v[188:191], v[4:7], v[80:83]
	ds_read_b64_tr_b16 v[190:191], v137 offset:57344
	v_mfma_f32_16x16x32_bf16 v[72:75], v[196:199], v[8:11], v[72:75]
	v_mfma_f32_16x16x32_bf16 v[72:75], v[204:207], v[12:15], v[72:75]
	s_waitcnt lgkmcnt(11)
	v_mfma_f32_16x16x32_bf16 v[80:83], v[208:211], v[0:3], 0
	ds_read_b64_tr_b16 v[188:189], v136 offset:57344
	ds_read_b64_tr_b16 v[196:197], v138 offset:49152
	ds_read_b64_tr_b16 v[198:199], v142 offset:49152
	ds_read_b64_tr_b16 v[206:207], v142 offset:57344
	v_mfma_f32_16x16x32_bf16 v[80:83], v[216:219], v[4:7], v[80:83]
	s_waitcnt lgkmcnt(11)
	v_mfma_f32_16x16x32_bf16 v[80:83], v[224:227], v[8:11], v[80:83]
	ds_read_b64_tr_b16 v[204:205], v138 offset:57344
	ds_read_b64_tr_b16 v[208:209], v139 offset:49152
	ds_read_b64_tr_b16 v[210:211], v143 offset:49152
	ds_read_b64_tr_b16 v[218:219], v143 offset:57344
	v_mfma_f32_16x16x32_bf16 v[84:87], v[88:91], v[12:15], v[80:83]
	v_mfma_f32_16x16x32_bf16 v[80:83], v[212:215], v[0:3], 0
	v_mfma_f32_16x16x32_bf16 v[80:83], v[220:223], v[4:7], v[80:83]
	s_waitcnt lgkmcnt(10)
	v_mfma_f32_16x16x32_bf16 v[48:51], v[156:159], v[68:71], v[48:51]
	ds_read_b64_tr_b16 v[216:217], v139 offset:57344
	ds_read_b64_tr_b16 v[224:225], v145 offset:49152
	ds_read_b64_tr_b16 v[226:227], v146 offset:49152
	ds_read_b64_tr_b16 v[90:91], v146 offset:57344
	ds_read_b64_tr_b16 v[88:89], v145 offset:57344
	v_mfma_f32_16x16x32_bf16 v[48:51], v[192:195], v[64:67], v[48:51]
	s_waitcnt lgkmcnt(11)
	v_mfma_f32_16x16x32_bf16 v[40:43], v[200:203], v[68:71], v[40:43]
	ds_read_b64_tr_b16 v[212:213], v147 offset:49152
	ds_read_b64_tr_b16 v[214:215], v148 offset:49152
	ds_read_b64_tr_b16 v[222:223], v148 offset:57344
	ds_read_b64_tr_b16 v[220:221], v147 offset:57344
	v_mfma_f32_16x16x32_bf16 v[40:43], v[188:191], v[64:67], v[40:43]
	s_waitcnt lgkmcnt(11)
	v_mfma_f32_16x16x32_bf16 v[44:47], v[196:199], v[68:71], v[44:47]
	ds_read_b64_tr_b16 v[156:157], v149 offset:49152
	ds_read_b64_tr_b16 v[158:159], v150 offset:49152
	ds_read_b64_tr_b16 v[194:195], v150 offset:57344
	ds_read_b64_tr_b16 v[192:193], v149 offset:57344
	v_mfma_f32_16x16x32_bf16 v[44:47], v[204:207], v[64:67], v[44:47]
	s_waitcnt lgkmcnt(11)
	v_mfma_f32_16x16x32_bf16 v[56:59], v[208:211], v[68:71], v[56:59]
	ds_read_b64_tr_b16 v[200:201], v151 offset:49152
	ds_read_b64_tr_b16 v[202:203], v152 offset:49152
	ds_read_b64_tr_b16 v[190:191], v152 offset:57344
	ds_read_b64_tr_b16 v[188:189], v151 offset:57344
	v_mfma_f32_16x16x32_bf16 v[56:59], v[216:219], v[64:67], v[56:59]
	s_waitcnt lgkmcnt(11)
	v_mfma_f32_16x16x32_bf16 v[60:63], v[224:227], v[68:71], v[60:63]
	v_mfma_f32_16x16x32_bf16 v[60:63], v[88:91], v[64:67], v[60:63]
	s_waitcnt lgkmcnt(7)
	v_mfma_f32_16x16x32_bf16 v[52:55], v[212:215], v[68:71], v[52:55]
	v_mfma_f32_16x16x32_bf16 v[52:55], v[220:223], v[64:67], v[52:55]
	s_waitcnt lgkmcnt(3)
	v_mfma_f32_16x16x32_bf16 v[32:35], v[156:159], v[68:71], v[32:35]
	v_mfma_f32_16x16x32_bf16 v[32:35], v[192:195], v[64:67], v[32:35]
	v_mfma_f32_16x16x32_bf16 v[80:83], v[228:231], v[8:11], v[80:83]
	s_waitcnt lgkmcnt(0)
	v_mfma_f32_16x16x32_bf16 v[36:39], v[200:203], v[68:71], v[36:39]
	v_mfma_f32_16x16x32_bf16 v[80:83], v[92:95], v[12:15], v[80:83]
	v_mfma_f32_16x16x32_bf16 v[36:39], v[188:191], v[64:67], v[36:39]
	s_cbranch_vccnz .LBB0_2032
	s_waitcnt vmcnt(3)
	ds_write_b128 v98, v[16:19] offset:16384
	s_waitcnt vmcnt(2)
	ds_write_b128 v99, v[20:23] offset:16384
	s_waitcnt vmcnt(1)
	ds_write_b128 v100, v[24:27] offset:32768
	s_waitcnt vmcnt(0)
	ds_write_b128 v124, v[28:31] offset:32768

.LBB0_2054:
	ds_read_b128 v[176:179], v128 offset:16384
	ds_read_b128 v[180:183], v128 offset:17408
	ds_read_b128 v[188:191], v129 offset:16384
	ds_read_b128 v[192:195], v130 offset:16384
	ds_read_b128 v[196:199], v131 offset:16384
	ds_read_b128 v[200:203], v129 offset:17408
	ds_read_b128 v[204:207], v130 offset:17408
	ds_read_b128 v[208:211], v129 offset:24576
	ds_read_b128 v[212:215], v131 offset:17408
	ds_read_b128 v[216:219], v128 offset:24576
	ds_read_b128 v[220:223], v130 offset:24576
	ds_read_b128 v[224:227], v128 offset:25600
	ds_read_b128 v[228:231], v131 offset:24576
	v_pk_mul_f32 v[184:185], v[66:67], v[68:69]
	s_waitcnt lgkmcnt(9)
	v_mfma_f32_16x16x32_bf16 v[160:163], v[176:179], v[0:3], 0
	ds_read_b128 v[176:179], v129 offset:25600
	v_mul_f32_e32 v70, v70, v71
	v_mul_f32_e32 v157, v70, v157
	v_mul_f32_e32 v159, v157, v159
	v_mfma_f32_16x16x32_bf16 v[164:167], v[180:183], v[0:3], 0
	ds_read_b128 v[180:183], v130 offset:25600
	v_mul_f32_e32 v186, v153, v159
	v_pk_mul_f32 v[64:65], v[64:65], v[96:97]
	v_pk_mul_f32 v[72:73], v[72:73], v[74:75]
	v_mfma_f32_16x16x32_bf16 v[160:163], v[188:191], v[4:7], v[160:163]
	ds_read_b128 v[188:191], v131 offset:25600
	v_pk_mul_f32 v[96:97], v[64:65], v[186:187] op_sel_hi:[1,0]
	v_pk_mul_f32 v[84:85], v[84:85], v[94:95]
	v_mfma_f32_16x16x32_bf16 v[66:69], v[192:195], v[8:11], v[160:163]
	ds_read_b64_tr_b16 v[192:193], v140 offset:32768
	ds_read_b64_tr_b16 v[194:195], v141 offset:32768
	v_cvt_pk_bf16_f32 v173, v96, v97
	v_pk_mul_f32 v[96:97], v[76:77], v[78:79]
	s_waitcnt lgkmcnt(10)
	v_mfma_f32_16x16x32_bf16 v[68:71], v[196:199], v[12:15], v[66:69]
	ds_read_b64_tr_b16 v[198:199], v141 offset:40960
	ds_read_b64_tr_b16 v[196:197], v140 offset:40960
	v_pk_mul_f32 v[96:97], v[96:97], v[186:187] op_sel_hi:[1,0]
	v_pk_mul_f32 v[86:87], v[86:87], v[92:93]
	v_mfma_f32_16x16x32_bf16 v[164:167], v[200:203], v[4:7], v[164:167]
	ds_read_b64_tr_b16 v[200:201], v136 offset:32768
	ds_read_b64_tr_b16 v[202:203], v137 offset:32768
	v_mul_f32_e64 v66, v184, v186
	v_mul_f32_e64 v67, v185, v186
	v_pk_mul_f32 v[80:81], v[80:81], v[82:83]
	v_cvt_pk_bf16_f32 v172, v66, v67
	v_mfma_f32_16x16x32_bf16 v[64:67], v[204:207], v[8:11], v[164:167]
	ds_read_b64_tr_b16 v[206:207], v137 offset:40960
	s_and_b64 vcc, exec, s[6:7]
	s_waitcnt lgkmcnt(11)
	v_mfma_f32_16x16x32_bf16 v[64:67], v[212:215], v[12:15], v[64:67]
	ds_read_b64_tr_b16 v[204:205], v136 offset:40960
	ds_read_b64_tr_b16 v[212:213], v138 offset:32768
	ds_read_b64_tr_b16 v[214:215], v142 offset:32768
	v_mfma_f32_16x16x32_bf16 v[168:171], v[216:219], v[0:3], 0
	ds_read_b64_tr_b16 v[218:219], v142 offset:40960
	v_cvt_pk_bf16_f32 v174, v96, v97
	v_pk_mul_f32 v[96:97], v[72:73], v[186:187] op_sel_hi:[1,0]
	v_mfma_f32_16x16x32_bf16 v[76:79], v[208:211], v[4:7], v[168:171]
	v_cvt_pk_bf16_f32 v175, v96, v97
	v_mfma_f32_16x16x32_bf16 v[94:97], v[224:227], v[0:3], 0
	v_mfma_f32_16x16x32_bf16 v[72:75], v[220:223], v[8:11], v[76:79]
	v_mul_f32_e32 v162, v153, v158
	v_pk_mul_f32 v[84:85], v[84:85], v[162:163] op_sel_hi:[1,0]
	v_pk_mul_f32 v[86:87], v[86:87], v[162:163] op_sel_hi:[1,0]
	s_waitcnt lgkmcnt(10)
	v_mfma_f32_16x16x32_bf16 v[92:95], v[176:179], v[4:7], v[94:97]
	ds_read_b64_tr_b16 v[216:217], v138 offset:40960
	ds_read_b64_tr_b16 v[208:209], v139 offset:32768
	ds_read_b64_tr_b16 v[210:211], v143 offset:32768
	ds_read_b64_tr_b16 v[226:227], v143 offset:40960
	ds_read_b64_tr_b16 v[224:225], v139 offset:40960
	v_cvt_pk_bf16_f32 v84, v84, v85
	v_cvt_pk_bf16_f32 v85, v86, v87
	v_pk_mul_f32 v[86:87], v[88:89], v[90:91]
	v_mfma_f32_16x16x32_bf16 v[92:95], v[180:183], v[8:11], v[92:95]
	v_pk_mul_f32 v[86:87], v[86:87], v[162:163] op_sel_hi:[1,0]
	v_mfma_f32_16x16x32_bf16 v[76:79], v[188:191], v[12:15], v[92:95]
	v_cvt_pk_bf16_f32 v86, v86, v87
	s_nop 4
	v_pk_mul_f32 v[92:93], v[80:81], v[162:163] op_sel_hi:[1,0]
	s_waitcnt lgkmcnt(11)
	v_mfma_f32_16x16x32_bf16 v[48:51], v[192:195], v[172:175], v[48:51]
	ds_read_b64_tr_b16 v[220:221], v145 offset:32768
	ds_read_b64_tr_b16 v[222:223], v146 offset:32768
	ds_read_b64_tr_b16 v[178:179], v146 offset:40960
	ds_read_b64_tr_b16 v[176:177], v145 offset:40960
	v_cvt_pk_bf16_f32 v87, v92, v93
	s_waitcnt lgkmcnt(11)
	v_mfma_f32_16x16x32_bf16 v[40:43], v[200:203], v[172:175], v[40:43]
	ds_read_b64_tr_b16 v[180:181], v147 offset:32768
	ds_read_b64_tr_b16 v[182:183], v148 offset:32768
	ds_read_b64_tr_b16 v[190:191], v148 offset:40960
	ds_read_b64_tr_b16 v[188:189], v147 offset:40960
	v_mfma_f32_16x16x32_bf16 v[40:43], v[204:207], v[84:87], v[40:43]
	s_waitcnt lgkmcnt(11)
	v_mfma_f32_16x16x32_bf16 v[44:47], v[212:215], v[172:175], v[44:47]
	ds_read_b64_tr_b16 v[192:193], v149 offset:32768
	ds_read_b64_tr_b16 v[194:195], v150 offset:32768
	ds_read_b64_tr_b16 v[202:203], v150 offset:40960
	ds_read_b64_tr_b16 v[200:201], v149 offset:40960
	v_mfma_f32_16x16x32_bf16 v[44:47], v[216:219], v[84:87], v[44:47]
	s_waitcnt lgkmcnt(11)
	v_mfma_f32_16x16x32_bf16 v[56:59], v[208:211], v[172:175], v[56:59]
	ds_read_b64_tr_b16 v[204:205], v151 offset:32768
	ds_read_b64_tr_b16 v[206:207], v152 offset:32768
	ds_read_b64_tr_b16 v[214:215], v152 offset:40960
	ds_read_b64_tr_b16 v[212:213], v151 offset:40960
	v_mfma_f32_16x16x32_bf16 v[56:59], v[224:227], v[84:87], v[56:59]
	s_waitcnt lgkmcnt(11)
	v_mfma_f32_16x16x32_bf16 v[60:63], v[220:223], v[172:175], v[60:63]
	v_mfma_f32_16x16x32_bf16 v[60:63], v[176:179], v[84:87], v[60:63]
	s_waitcnt lgkmcnt(7)
	v_mfma_f32_16x16x32_bf16 v[52:55], v[180:183], v[172:175], v[52:55]
	v_mfma_f32_16x16x32_bf16 v[52:55], v[188:191], v[84:87], v[52:55]
	s_waitcnt lgkmcnt(3)
	v_mfma_f32_16x16x32_bf16 v[32:35], v[192:195], v[172:175], v[32:35]
	v_mfma_f32_16x16x32_bf16 v[32:35], v[200:203], v[84:87], v[32:35]
	s_waitcnt lgkmcnt(0)
	v_mfma_f32_16x16x32_bf16 v[36:39], v[204:207], v[172:175], v[36:39]
	v_mfma_f32_16x16x32_bf16 v[72:75], v[228:231], v[12:15], v[72:75]
	v_mfma_f32_16x16x32_bf16 v[48:51], v[196:199], v[84:87], v[48:51]
	v_mfma_f32_16x16x32_bf16 v[36:39], v[212:215], v[84:87], v[36:39]
	s_cbranch_vccnz .LBB0_2056
	s_waitcnt vmcnt(3)
	ds_write_b128 v98, v[16:19]
	s_waitcnt vmcnt(2)
	ds_write_b128 v99, v[20:23]
	s_waitcnt vmcnt(1)
	ds_write_b128 v100, v[24:27] offset:49152
	s_waitcnt vmcnt(0)
	ds_write_b128 v124, v[28:31] offset:49152

.LBB0_2133:
	ds_read_b128 v[88:91], v128
	ds_read_b128 v[92:95], v128 offset:1024
	ds_read_b128 v[156:159], v129
	ds_read_b128 v[188:191], v129 offset:1024
	ds_read_b128 v[192:195], v130
	ds_read_b128 v[196:199], v130 offset:1024
	ds_read_b128 v[200:203], v131
	ds_read_b128 v[204:207], v131 offset:1024
	ds_read_b128 v[208:211], v128 offset:8192
	ds_read_b128 v[212:215], v128 offset:9216
	ds_read_b128 v[216:219], v129 offset:8192
	ds_read_b128 v[220:223], v129 offset:9216
	ds_read_b128 v[224:227], v130 offset:8192
	ds_read_b128 v[228:231], v130 offset:9216
	s_and_b64 vcc, exec, s[6:7]
	s_waitcnt lgkmcnt(10)
	v_mfma_f32_16x16x32_bf16 v[72:75], v[88:91], v[0:3], 0
	ds_read_b128 v[88:91], v131 offset:8192
	v_mfma_f32_16x16x32_bf16 v[80:83], v[92:95], v[0:3], 0
	ds_read_b128 v[92:95], v131 offset:9216
	v_mfma_f32_16x16x32_bf16 v[72:75], v[156:159], v[4:7], v[72:75]
	ds_read_b64_tr_b16 v[156:157], v142 offset:49152
	ds_read_b64_tr_b16 v[158:159], v143 offset:49152
	s_waitcnt lgkmcnt(10)
	v_mfma_f32_16x16x32_bf16 v[72:75], v[192:195], v[8:11], v[72:75]
	ds_read_b64_tr_b16 v[194:195], v143 offset:57344
	ds_read_b64_tr_b16 v[192:193], v142 offset:57344
	v_mfma_f32_16x16x32_bf16 v[76:79], v[200:203], v[12:15], v[72:75]
	ds_read_b64_tr_b16 v[200:201], v136 offset:49152
	ds_read_b64_tr_b16 v[202:203], v139 offset:49152
	v_mfma_f32_16x16x32_bf16 v[72:75], v[188:191], v[4:7], v[80:83]
	ds_read_b64_tr_b16 v[190:191], v139 offset:57344
	v_mfma_f32_16x16x32_bf16 v[72:75], v[196:199], v[8:11], v[72:75]
	v_mfma_f32_16x16x32_bf16 v[72:75], v[204:207], v[12:15], v[72:75]
	s_waitcnt lgkmcnt(11)
	v_mfma_f32_16x16x32_bf16 v[80:83], v[208:211], v[0:3], 0
	ds_read_b64_tr_b16 v[188:189], v136 offset:57344
	ds_read_b64_tr_b16 v[196:197], v138 offset:49152
	ds_read_b64_tr_b16 v[198:199], v141 offset:49152
	ds_read_b64_tr_b16 v[206:207], v141 offset:57344
	v_mfma_f32_16x16x32_bf16 v[80:83], v[216:219], v[4:7], v[80:83]
	s_waitcnt lgkmcnt(11)
	v_mfma_f32_16x16x32_bf16 v[80:83], v[224:227], v[8:11], v[80:83]
	ds_read_b64_tr_b16 v[204:205], v138 offset:57344
	ds_read_b64_tr_b16 v[208:209], v137 offset:49152
	ds_read_b64_tr_b16 v[210:211], v140 offset:49152
	ds_read_b64_tr_b16 v[218:219], v140 offset:57344
	v_mfma_f32_16x16x32_bf16 v[84:87], v[88:91], v[12:15], v[80:83]
	v_mfma_f32_16x16x32_bf16 v[80:83], v[212:215], v[0:3], 0
	v_mfma_f32_16x16x32_bf16 v[80:83], v[220:223], v[4:7], v[80:83]
	s_waitcnt lgkmcnt(10)
	v_mfma_f32_16x16x32_bf16 v[60:63], v[156:159], v[64:67], v[60:63]
	ds_read_b64_tr_b16 v[216:217], v137 offset:57344
	ds_read_b64_tr_b16 v[224:225], v145 offset:49152
	ds_read_b64_tr_b16 v[226:227], v146 offset:49152
	ds_read_b64_tr_b16 v[90:91], v146 offset:57344
	ds_read_b64_tr_b16 v[88:89], v145 offset:57344
	v_mfma_f32_16x16x32_bf16 v[60:63], v[192:195], v[68:71], v[60:63]
	s_waitcnt lgkmcnt(11)
	v_mfma_f32_16x16x32_bf16 v[52:55], v[200:203], v[64:67], v[52:55]
	ds_read_b64_tr_b16 v[212:213], v147 offset:49152
	ds_read_b64_tr_b16 v[214:215], v148 offset:49152
	ds_read_b64_tr_b16 v[222:223], v148 offset:57344
	ds_read_b64_tr_b16 v[220:221], v147 offset:57344
	v_mfma_f32_16x16x32_bf16 v[52:55], v[188:191], v[68:71], v[52:55]
	s_waitcnt lgkmcnt(11)
	v_mfma_f32_16x16x32_bf16 v[44:47], v[196:199], v[64:67], v[44:47]
	ds_read_b64_tr_b16 v[156:157], v149 offset:49152
	ds_read_b64_tr_b16 v[158:159], v150 offset:49152
	ds_read_b64_tr_b16 v[194:195], v150 offset:57344
	ds_read_b64_tr_b16 v[192:193], v149 offset:57344
	v_mfma_f32_16x16x32_bf16 v[44:47], v[204:207], v[68:71], v[44:47]
	s_waitcnt lgkmcnt(11)
	v_mfma_f32_16x16x32_bf16 v[56:59], v[208:211], v[64:67], v[56:59]
	ds_read_b64_tr_b16 v[200:201], v151 offset:49152
	ds_read_b64_tr_b16 v[202:203], v152 offset:49152
	ds_read_b64_tr_b16 v[190:191], v152 offset:57344
	ds_read_b64_tr_b16 v[188:189], v151 offset:57344
	v_mfma_f32_16x16x32_bf16 v[56:59], v[216:219], v[68:71], v[56:59]
	s_waitcnt lgkmcnt(11)
	v_mfma_f32_16x16x32_bf16 v[48:51], v[224:227], v[64:67], v[48:51]
	v_mfma_f32_16x16x32_bf16 v[48:51], v[88:91], v[68:71], v[48:51]
	s_waitcnt lgkmcnt(7)
	v_mfma_f32_16x16x32_bf16 v[40:43], v[212:215], v[64:67], v[40:43]
	v_mfma_f32_16x16x32_bf16 v[40:43], v[220:223], v[68:71], v[40:43]
	s_waitcnt lgkmcnt(3)
	v_mfma_f32_16x16x32_bf16 v[32:35], v[156:159], v[64:67], v[32:35]
	v_mfma_f32_16x16x32_bf16 v[32:35], v[192:195], v[68:71], v[32:35]
	v_mfma_f32_16x16x32_bf16 v[80:83], v[228:231], v[8:11], v[80:83]
	s_waitcnt lgkmcnt(0)
	v_mfma_f32_16x16x32_bf16 v[36:39], v[200:203], v[64:67], v[36:39]
	v_mfma_f32_16x16x32_bf16 v[80:83], v[92:95], v[12:15], v[80:83]
	v_mfma_f32_16x16x32_bf16 v[36:39], v[188:191], v[68:71], v[36:39]
	s_cbranch_vccnz .LBB0_2135
	s_waitcnt vmcnt(3)
	ds_write_b128 v98, v[16:19] offset:16384
	s_waitcnt vmcnt(2)
	ds_write_b128 v99, v[20:23] offset:16384
	s_waitcnt vmcnt(1)
	ds_write_b128 v100, v[24:27] offset:32768
	s_waitcnt vmcnt(0)
	ds_write_b128 v124, v[28:31] offset:32768

.LBB0_2157:
	ds_read_b128 v[176:179], v128 offset:16384
	ds_read_b128 v[180:183], v128 offset:17408
	ds_read_b128 v[188:191], v129 offset:16384
	ds_read_b128 v[192:195], v130 offset:16384
	ds_read_b128 v[196:199], v131 offset:16384
	ds_read_b128 v[200:203], v129 offset:17408
	ds_read_b128 v[204:207], v130 offset:17408
	ds_read_b128 v[208:211], v129 offset:24576
	ds_read_b128 v[212:215], v131 offset:17408
	ds_read_b128 v[216:219], v128 offset:24576
	ds_read_b128 v[220:223], v130 offset:24576
	ds_read_b128 v[224:227], v128 offset:25600
	ds_read_b128 v[228:231], v131 offset:24576
	v_pk_mul_f32 v[184:185], v[66:67], v[68:69]
	s_waitcnt lgkmcnt(9)
	v_mfma_f32_16x16x32_bf16 v[160:163], v[176:179], v[0:3], 0
	ds_read_b128 v[176:179], v129 offset:25600
	v_mul_f32_e32 v70, v70, v71
	v_mul_f32_e32 v157, v70, v157
	v_mul_f32_e32 v159, v157, v159
	v_mfma_f32_16x16x32_bf16 v[164:167], v[180:183], v[0:3], 0
	ds_read_b128 v[180:183], v130 offset:25600
	v_mul_f32_e32 v186, v153, v159
	v_pk_mul_f32 v[64:65], v[64:65], v[96:97]
	v_pk_mul_f32 v[72:73], v[72:73], v[74:75]
	v_mfma_f32_16x16x32_bf16 v[160:163], v[188:191], v[4:7], v[160:163]
	ds_read_b128 v[188:191], v131 offset:25600
	v_pk_mul_f32 v[96:97], v[64:65], v[186:187] op_sel_hi:[1,0]
	v_pk_mul_f32 v[84:85], v[84:85], v[94:95]
	v_mfma_f32_16x16x32_bf16 v[66:69], v[192:195], v[8:11], v[160:163]
	ds_read_b64_tr_b16 v[192:193], v142 offset:32768
	ds_read_b64_tr_b16 v[194:195], v143 offset:32768
	v_cvt_pk_bf16_f32 v173, v96, v97
	v_pk_mul_f32 v[96:97], v[76:77], v[78:79]
	s_waitcnt lgkmcnt(10)
	v_mfma_f32_16x16x32_bf16 v[68:71], v[196:199], v[12:15], v[66:69]
	ds_read_b64_tr_b16 v[198:199], v143 offset:40960
	ds_read_b64_tr_b16 v[196:197], v142 offset:40960
	v_pk_mul_f32 v[96:97], v[96:97], v[186:187] op_sel_hi:[1,0]
	v_pk_mul_f32 v[86:87], v[86:87], v[92:93]
	v_mfma_f32_16x16x32_bf16 v[164:167], v[200:203], v[4:7], v[164:167]
	ds_read_b64_tr_b16 v[200:201], v136 offset:32768
	ds_read_b64_tr_b16 v[202:203], v139 offset:32768
	v_mul_f32_e64 v66, v184, v186
	v_mul_f32_e64 v67, v185, v186
	v_pk_mul_f32 v[80:81], v[80:81], v[82:83]
	v_cvt_pk_bf16_f32 v172, v66, v67
	v_mfma_f32_16x16x32_bf16 v[64:67], v[204:207], v[8:11], v[164:167]
	ds_read_b64_tr_b16 v[206:207], v139 offset:40960
	s_and_b64 vcc, exec, s[6:7]
	s_waitcnt lgkmcnt(11)
	v_mfma_f32_16x16x32_bf16 v[64:67], v[212:215], v[12:15], v[64:67]
	ds_read_b64_tr_b16 v[204:205], v136 offset:40960
	ds_read_b64_tr_b16 v[212:213], v138 offset:32768
	ds_read_b64_tr_b16 v[214:215], v141 offset:32768
	v_mfma_f32_16x16x32_bf16 v[168:171], v[216:219], v[0:3], 0
	ds_read_b64_tr_b16 v[218:219], v141 offset:40960
	v_cvt_pk_bf16_f32 v174, v96, v97
	v_pk_mul_f32 v[96:97], v[72:73], v[186:187] op_sel_hi:[1,0]
	v_mfma_f32_16x16x32_bf16 v[76:79], v[208:211], v[4:7], v[168:171]
	v_cvt_pk_bf16_f32 v175, v96, v97
	v_mfma_f32_16x16x32_bf16 v[94:97], v[224:227], v[0:3], 0
	v_mfma_f32_16x16x32_bf16 v[72:75], v[220:223], v[8:11], v[76:79]
	v_mul_f32_e32 v162, v153, v158
	v_pk_mul_f32 v[84:85], v[84:85], v[162:163] op_sel_hi:[1,0]
	v_pk_mul_f32 v[86:87], v[86:87], v[162:163] op_sel_hi:[1,0]
	s_waitcnt lgkmcnt(10)
	v_mfma_f32_16x16x32_bf16 v[92:95], v[176:179], v[4:7], v[94:97]
	ds_read_b64_tr_b16 v[216:217], v138 offset:40960
	ds_read_b64_tr_b16 v[208:209], v137 offset:32768
	ds_read_b64_tr_b16 v[210:211], v140 offset:32768
	ds_read_b64_tr_b16 v[226:227], v140 offset:40960
	ds_read_b64_tr_b16 v[224:225], v137 offset:40960
	v_cvt_pk_bf16_f32 v84, v84, v85
	v_cvt_pk_bf16_f32 v85, v86, v87
	v_pk_mul_f32 v[86:87], v[88:89], v[90:91]
	v_mfma_f32_16x16x32_bf16 v[92:95], v[180:183], v[8:11], v[92:95]
	v_pk_mul_f32 v[86:87], v[86:87], v[162:163] op_sel_hi:[1,0]
	v_mfma_f32_16x16x32_bf16 v[76:79], v[188:191], v[12:15], v[92:95]
	v_cvt_pk_bf16_f32 v86, v86, v87
	s_nop 4
	v_pk_mul_f32 v[92:93], v[80:81], v[162:163] op_sel_hi:[1,0]
	s_waitcnt lgkmcnt(11)
	v_mfma_f32_16x16x32_bf16 v[60:63], v[192:195], v[172:175], v[60:63]
	ds_read_b64_tr_b16 v[220:221], v145 offset:32768
	ds_read_b64_tr_b16 v[222:223], v146 offset:32768
	ds_read_b64_tr_b16 v[178:179], v146 offset:40960
	ds_read_b64_tr_b16 v[176:177], v145 offset:40960
	v_cvt_pk_bf16_f32 v87, v92, v93
	s_waitcnt lgkmcnt(11)
	v_mfma_f32_16x16x32_bf16 v[52:55], v[200:203], v[172:175], v[52:55]
	ds_read_b64_tr_b16 v[180:181], v147 offset:32768
	ds_read_b64_tr_b16 v[182:183], v148 offset:32768
	ds_read_b64_tr_b16 v[190:191], v148 offset:40960
	ds_read_b64_tr_b16 v[188:189], v147 offset:40960
	v_mfma_f32_16x16x32_bf16 v[52:55], v[204:207], v[84:87], v[52:55]
	s_waitcnt lgkmcnt(11)
	v_mfma_f32_16x16x32_bf16 v[44:47], v[212:215], v[172:175], v[44:47]
	ds_read_b64_tr_b16 v[192:193], v149 offset:32768
	ds_read_b64_tr_b16 v[194:195], v150 offset:32768
	ds_read_b64_tr_b16 v[202:203], v150 offset:40960
	ds_read_b64_tr_b16 v[200:201], v149 offset:40960
	v_mfma_f32_16x16x32_bf16 v[44:47], v[216:219], v[84:87], v[44:47]
	s_waitcnt lgkmcnt(11)
	v_mfma_f32_16x16x32_bf16 v[56:59], v[208:211], v[172:175], v[56:59]
	ds_read_b64_tr_b16 v[204:205], v151 offset:32768
	ds_read_b64_tr_b16 v[206:207], v152 offset:32768
	ds_read_b64_tr_b16 v[214:215], v152 offset:40960
	ds_read_b64_tr_b16 v[212:213], v151 offset:40960
	v_mfma_f32_16x16x32_bf16 v[56:59], v[224:227], v[84:87], v[56:59]
	s_waitcnt lgkmcnt(11)
	v_mfma_f32_16x16x32_bf16 v[48:51], v[220:223], v[172:175], v[48:51]
	v_mfma_f32_16x16x32_bf16 v[48:51], v[176:179], v[84:87], v[48:51]
	s_waitcnt lgkmcnt(7)
	v_mfma_f32_16x16x32_bf16 v[40:43], v[180:183], v[172:175], v[40:43]
	v_mfma_f32_16x16x32_bf16 v[40:43], v[188:191], v[84:87], v[40:43]
	s_waitcnt lgkmcnt(3)
	v_mfma_f32_16x16x32_bf16 v[32:35], v[192:195], v[172:175], v[32:35]
	v_mfma_f32_16x16x32_bf16 v[32:35], v[200:203], v[84:87], v[32:35]
	s_waitcnt lgkmcnt(0)
	v_mfma_f32_16x16x32_bf16 v[36:39], v[204:207], v[172:175], v[36:39]
	v_mfma_f32_16x16x32_bf16 v[72:75], v[228:231], v[12:15], v[72:75]
	v_mfma_f32_16x16x32_bf16 v[60:63], v[196:199], v[84:87], v[60:63]
	v_mfma_f32_16x16x32_bf16 v[36:39], v[212:215], v[84:87], v[36:39]
	s_cbranch_vccnz .LBB0_2159
	s_waitcnt vmcnt(3)
	ds_write_b128 v98, v[16:19]
	s_waitcnt vmcnt(2)
	ds_write_b128 v99, v[20:23]
	s_waitcnt vmcnt(1)
	ds_write_b128 v100, v[24:27] offset:49152
	s_waitcnt vmcnt(0)
	ds_write_b128 v124, v[28:31] offset:49152
